# final_d with sc1 (write-through) stores in the barrier-hosted tile conversion
# baseline (speedup 1.0000x reference)
.Lhw_go_s0_0:
	s_add_u32 s100, s82, s69
	s_addc_u32 s101, s83, 0
	v_readlane_b32 s82, v239, 44
	v_readlane_b32 s83, v239, 45
	s_add_u32 s82, s82, s98
	s_addc_u32 s83, s83, 0
	global_load_dword v34, v178, s[100:101] nt
	s_add_u32 s100, s100, s89
	s_addc_u32 s101, s101, 0
	global_load_dword v35, v178, s[100:101] nt
	s_add_u32 s100, s100, s89
	s_addc_u32 s101, s101, 0
	global_load_dword v36, v178, s[100:101] nt
	s_add_u32 s100, s100, s89
	s_addc_u32 s101, s101, 0
	global_load_dword v37, v178, s[100:101] nt
	s_add_u32 s100, s100, s89
	s_addc_u32 s101, s101, 0
	global_load_dword v38, v178, s[100:101] nt
	s_add_u32 s100, s100, s89
	s_addc_u32 s101, s101, 0
	global_load_dword v39, v178, s[100:101] nt
	s_add_u32 s100, s100, s89
	s_addc_u32 s101, s101, 0
	global_load_dword v40, v178, s[100:101] nt
	s_add_u32 s100, s100, s89
	s_addc_u32 s101, s101, 0
	global_load_dword v41, v178, s[100:101] nt
	s_add_u32 s100, s100, s89
	s_addc_u32 s101, s101, 0
	global_load_dword v42, v178, s[100:101] nt
	s_add_u32 s100, s100, s89
	s_addc_u32 s101, s101, 0
	global_load_dword v43, v178, s[100:101] nt
	s_add_u32 s100, s100, s89
	s_addc_u32 s101, s101, 0
	global_load_dword v44, v178, s[100:101] nt
	s_add_u32 s100, s100, s89
	s_addc_u32 s101, s101, 0
	global_load_dword v45, v178, s[100:101] nt
	s_add_u32 s100, s100, s89
	s_addc_u32 s101, s101, 0
	global_load_dword v46, v178, s[100:101] nt
	s_add_u32 s100, s100, s89
	s_addc_u32 s101, s101, 0
	global_load_dword v47, v178, s[100:101] nt
	s_add_u32 s100, s100, s89
	s_addc_u32 s101, s101, 0
	global_load_dword v48, v178, s[100:101] nt
	s_add_u32 s100, s100, s89
	s_addc_u32 s101, s101, 0
	global_load_dword v49, v178, s[100:101] nt
	s_add_u32 s100, s100, s89
	s_addc_u32 s101, s101, 0
	global_load_dword v50, v178, s[100:101] nt
	s_add_u32 s100, s100, s89
	s_addc_u32 s101, s101, 0
	global_load_dword v51, v178, s[100:101] nt
	s_add_u32 s100, s100, s89
	s_addc_u32 s101, s101, 0
	global_load_dword v52, v178, s[100:101] nt
	s_add_u32 s100, s100, s89
	s_addc_u32 s101, s101, 0
	global_load_dword v53, v178, s[100:101] nt
	s_add_u32 s100, s100, s89
	s_addc_u32 s101, s101, 0
	global_load_dword v54, v178, s[100:101] nt
	s_add_u32 s100, s100, s89
	s_addc_u32 s101, s101, 0
	global_load_dword v55, v178, s[100:101] nt
	s_add_u32 s100, s100, s89
	s_addc_u32 s101, s101, 0
	global_load_dword v56, v178, s[100:101] nt
	s_add_u32 s100, s100, s89
	s_addc_u32 s101, s101, 0
	global_load_dword v57, v178, s[100:101] nt
	s_add_u32 s100, s100, s89
	s_addc_u32 s101, s101, 0
	global_load_dword v58, v178, s[100:101] nt
	s_add_u32 s100, s100, s89
	s_addc_u32 s101, s101, 0
	global_load_dword v59, v178, s[100:101] nt
	s_add_u32 s100, s100, s89
	s_addc_u32 s101, s101, 0
	global_load_dword v60, v178, s[100:101] nt
	s_add_u32 s100, s100, s89
	s_addc_u32 s101, s101, 0
	global_load_dword v61, v178, s[100:101] nt
	s_add_u32 s100, s100, s89
	s_addc_u32 s101, s101, 0
	global_load_dword v62, v178, s[100:101] nt
	s_add_u32 s100, s100, s89
	s_addc_u32 s101, s101, 0
	global_load_dword v63, v178, s[100:101] nt
	s_add_u32 s100, s100, s89
	s_addc_u32 s101, s101, 0
	global_load_dword v64, v178, s[100:101] nt
	s_add_u32 s100, s100, s89
	s_addc_u32 s101, s101, 0
	global_load_dword v65, v178, s[100:101] nt
	s_add_u32 s100, s100, s89
	s_addc_u32 s101, s101, 0
	global_load_dword v66, v178, s[100:101] nt
	s_add_u32 s100, s100, s89
	s_addc_u32 s101, s101, 0
	global_load_dword v67, v178, s[100:101] nt
	s_add_u32 s100, s100, s89
	s_addc_u32 s101, s101, 0
	global_load_dword v68, v178, s[100:101] nt
	s_add_u32 s100, s100, s89
	s_addc_u32 s101, s101, 0
	global_load_dword v69, v178, s[100:101] nt
	s_add_u32 s100, s100, s89
	s_addc_u32 s101, s101, 0
	global_load_dword v70, v178, s[100:101] nt
	s_add_u32 s100, s100, s89
	s_addc_u32 s101, s101, 0
	global_load_dword v71, v178, s[100:101] nt
	s_add_u32 s100, s100, s89
	s_addc_u32 s101, s101, 0
	global_load_dword v72, v178, s[100:101] nt
	s_add_u32 s100, s100, s89
	s_addc_u32 s101, s101, 0
	global_load_dword v73, v178, s[100:101] nt
	s_add_u32 s100, s100, s89
	s_addc_u32 s101, s101, 0
	global_load_dword v74, v178, s[100:101] nt
	s_add_u32 s100, s100, s89
	s_addc_u32 s101, s101, 0
	global_load_dword v75, v178, s[100:101] nt
	s_add_u32 s100, s100, s89
	s_addc_u32 s101, s101, 0
	global_load_dword v76, v178, s[100:101] nt
	s_add_u32 s100, s100, s89
	s_addc_u32 s101, s101, 0
	global_load_dword v77, v178, s[100:101] nt
	s_add_u32 s100, s100, s89
	s_addc_u32 s101, s101, 0
	global_load_dword v78, v178, s[100:101] nt
	s_add_u32 s100, s100, s89
	s_addc_u32 s101, s101, 0
	global_load_dword v79, v178, s[100:101] nt
	s_add_u32 s100, s100, s89
	s_addc_u32 s101, s101, 0
	global_load_dword v80, v178, s[100:101] nt
	s_add_u32 s100, s100, s89
	s_addc_u32 s101, s101, 0
	global_load_dword v81, v178, s[100:101] nt
	s_add_u32 s100, s100, s89
	s_addc_u32 s101, s101, 0
	global_load_dword v82, v178, s[100:101] nt
	s_add_u32 s100, s100, s89
	s_addc_u32 s101, s101, 0
	global_load_dword v83, v178, s[100:101] nt
	s_add_u32 s100, s100, s89
	s_addc_u32 s101, s101, 0
	global_load_dword v84, v178, s[100:101] nt
	s_add_u32 s100, s100, s89
	s_addc_u32 s101, s101, 0
	global_load_dword v85, v178, s[100:101] nt
	s_add_u32 s100, s100, s89
	s_addc_u32 s101, s101, 0
	global_load_dword v86, v178, s[100:101] nt
	s_add_u32 s100, s100, s89
	s_addc_u32 s101, s101, 0
	global_load_dword v87, v178, s[100:101] nt
	s_add_u32 s100, s100, s89
	s_addc_u32 s101, s101, 0
	global_load_dword v88, v178, s[100:101] nt
	s_add_u32 s100, s100, s89
	s_addc_u32 s101, s101, 0
	global_load_dword v89, v178, s[100:101] nt
	s_add_u32 s100, s100, s89
	s_addc_u32 s101, s101, 0
	global_load_dword v90, v178, s[100:101] nt
	s_add_u32 s100, s100, s89
	s_addc_u32 s101, s101, 0
	global_load_dword v91, v178, s[100:101] nt
	s_add_u32 s100, s100, s89
	s_addc_u32 s101, s101, 0
	global_load_dword v92, v178, s[100:101] nt
	s_add_u32 s100, s100, s89
	s_addc_u32 s101, s101, 0
	global_load_dword v93, v178, s[100:101] nt
	s_add_u32 s100, s100, s89
	s_addc_u32 s101, s101, 0
	global_load_dword v94, v178, s[100:101] nt
	s_add_u32 s100, s100, s89
	s_addc_u32 s101, s101, 0
	global_load_dword v95, v178, s[100:101] nt
	s_add_u32 s100, s100, s89
	s_addc_u32 s101, s101, 0
	global_load_dword v96, v178, s[100:101] nt
	s_add_u32 s100, s100, s89
	s_addc_u32 s101, s101, 0
	global_load_dword v97, v178, s[100:101] nt
	s_add_u32 s100, s100, s89
	s_addc_u32 s101, s101, 0
	s_waitcnt vmcnt(48)
	v_mul_f32_e32 v34, 0x42000000, v34
	v_mul_f32_e32 v35, 0x42000000, v35
	v_mul_f32_e32 v36, 0x42000000, v36
	v_mul_f32_e32 v37, 0x42000000, v37
	v_mul_f32_e32 v38, 0x42000000, v38
	v_mul_f32_e32 v39, 0x42000000, v39
	v_mul_f32_e32 v40, 0x42000000, v40
	v_mul_f32_e32 v41, 0x42000000, v41
	v_mul_f32_e32 v42, 0x42000000, v42
	v_mul_f32_e32 v43, 0x42000000, v43
	v_mul_f32_e32 v44, 0x42000000, v44
	v_mul_f32_e32 v45, 0x42000000, v45
	v_mul_f32_e32 v46, 0x42000000, v46
	v_mul_f32_e32 v47, 0x42000000, v47
	v_mul_f32_e32 v48, 0x42000000, v48
	v_mul_f32_e32 v49, 0x42000000, v49
	v_cvt_pk_fp8_f32 v154, v34, v35
	v_cvt_pk_fp8_f32 v155, v38, v39
	v_cvt_pk_fp8_f32 v156, v42, v43
	v_cvt_pk_fp8_f32 v157, v46, v47
	v_cvt_pk_fp8_f32 v154, v36, v37 op_sel:[0,0,1]
	v_cvt_pk_fp8_f32 v155, v40, v41 op_sel:[0,0,1]
	v_cvt_pk_fp8_f32 v156, v44, v45 op_sel:[0,0,1]
	v_cvt_pk_fp8_f32 v157, v48, v49 op_sel:[0,0,1]
	s_waitcnt vmcnt(32)
	v_mul_f32_e32 v50, 0x42000000, v50
	v_mul_f32_e32 v51, 0x42000000, v51
	v_mul_f32_e32 v52, 0x42000000, v52
	v_mul_f32_e32 v53, 0x42000000, v53
	v_mul_f32_e32 v54, 0x42000000, v54
	v_mul_f32_e32 v55, 0x42000000, v55
	v_mul_f32_e32 v56, 0x42000000, v56
	v_mul_f32_e32 v57, 0x42000000, v57
	v_mul_f32_e32 v58, 0x42000000, v58
	v_mul_f32_e32 v59, 0x42000000, v59
	v_mul_f32_e32 v60, 0x42000000, v60
	v_mul_f32_e32 v61, 0x42000000, v61
	v_mul_f32_e32 v62, 0x42000000, v62
	v_mul_f32_e32 v63, 0x42000000, v63
	v_mul_f32_e32 v64, 0x42000000, v64
	v_mul_f32_e32 v65, 0x42000000, v65
	v_cvt_pk_fp8_f32 v158, v50, v51
	v_cvt_pk_fp8_f32 v159, v54, v55
	v_cvt_pk_fp8_f32 v160, v58, v59
	v_cvt_pk_fp8_f32 v161, v62, v63
	v_cvt_pk_fp8_f32 v158, v52, v53 op_sel:[0,0,1]
	v_cvt_pk_fp8_f32 v159, v56, v57 op_sel:[0,0,1]
	v_cvt_pk_fp8_f32 v160, v60, v61 op_sel:[0,0,1]
	v_cvt_pk_fp8_f32 v161, v64, v65 op_sel:[0,0,1]
	s_waitcnt vmcnt(16)
	v_mul_f32_e32 v66, 0x42000000, v66
	v_mul_f32_e32 v67, 0x42000000, v67
	v_mul_f32_e32 v68, 0x42000000, v68
	v_mul_f32_e32 v69, 0x42000000, v69
	v_mul_f32_e32 v70, 0x42000000, v70
	v_mul_f32_e32 v71, 0x42000000, v71
	v_mul_f32_e32 v72, 0x42000000, v72
	v_mul_f32_e32 v73, 0x42000000, v73
	v_mul_f32_e32 v74, 0x42000000, v74
	v_mul_f32_e32 v75, 0x42000000, v75
	v_mul_f32_e32 v76, 0x42000000, v76
	v_mul_f32_e32 v77, 0x42000000, v77
	v_mul_f32_e32 v78, 0x42000000, v78
	v_mul_f32_e32 v79, 0x42000000, v79
	v_mul_f32_e32 v80, 0x42000000, v80
	v_mul_f32_e32 v81, 0x42000000, v81
	v_cvt_pk_fp8_f32 v162, v66, v67
	v_cvt_pk_fp8_f32 v163, v70, v71
	v_cvt_pk_fp8_f32 v164, v74, v75
	v_cvt_pk_fp8_f32 v165, v78, v79
	v_cvt_pk_fp8_f32 v162, v68, v69 op_sel:[0,0,1]
	v_cvt_pk_fp8_f32 v163, v72, v73 op_sel:[0,0,1]
	v_cvt_pk_fp8_f32 v164, v76, v77 op_sel:[0,0,1]
	v_cvt_pk_fp8_f32 v165, v80, v81 op_sel:[0,0,1]
	s_waitcnt vmcnt(0)
	v_mul_f32_e32 v82, 0x42000000, v82
	v_mul_f32_e32 v83, 0x42000000, v83
	v_mul_f32_e32 v84, 0x42000000, v84
	v_mul_f32_e32 v85, 0x42000000, v85
	v_mul_f32_e32 v86, 0x42000000, v86
	v_mul_f32_e32 v87, 0x42000000, v87
	v_mul_f32_e32 v88, 0x42000000, v88
	v_mul_f32_e32 v89, 0x42000000, v89
	v_mul_f32_e32 v90, 0x42000000, v90
	v_mul_f32_e32 v91, 0x42000000, v91
	v_mul_f32_e32 v92, 0x42000000, v92
	v_mul_f32_e32 v93, 0x42000000, v93
	v_mul_f32_e32 v94, 0x42000000, v94
	v_mul_f32_e32 v95, 0x42000000, v95
	v_mul_f32_e32 v96, 0x42000000, v96
	v_mul_f32_e32 v97, 0x42000000, v97
	v_cvt_pk_fp8_f32 v166, v82, v83
	v_cvt_pk_fp8_f32 v167, v86, v87
	v_cvt_pk_fp8_f32 v168, v90, v91
	v_cvt_pk_fp8_f32 v169, v94, v95
	v_cvt_pk_fp8_f32 v166, v84, v85 op_sel:[0,0,1]
	v_cvt_pk_fp8_f32 v167, v88, v89 op_sel:[0,0,1]
	v_cvt_pk_fp8_f32 v168, v92, v93 op_sel:[0,0,1]
	v_cvt_pk_fp8_f32 v169, v96, v97 op_sel:[0,0,1]
	s_mov_b32 vcc_lo, 0xaaaaaaaa
	s_mov_b32 vcc_hi, 0xaaaaaaaa
	s_nop 1
	v_cndmask_b32_dpp v170, v154, v158, vcc quad_perm:[1,0,3,2] row_mask:0xf bank_mask:0xf
	v_cndmask_b32_dpp v174, v162, v166, vcc quad_perm:[1,0,3,2] row_mask:0xf bank_mask:0xf
	v_cndmask_b32_dpp v171, v155, v159, vcc quad_perm:[1,0,3,2] row_mask:0xf bank_mask:0xf
	v_cndmask_b32_dpp v175, v163, v167, vcc quad_perm:[1,0,3,2] row_mask:0xf bank_mask:0xf
	v_cndmask_b32_dpp v172, v156, v160, vcc quad_perm:[1,0,3,2] row_mask:0xf bank_mask:0xf
	v_cndmask_b32_dpp v176, v164, v168, vcc quad_perm:[1,0,3,2] row_mask:0xf bank_mask:0xf
	v_cndmask_b32_dpp v173, v157, v161, vcc quad_perm:[1,0,3,2] row_mask:0xf bank_mask:0xf
	v_cndmask_b32_dpp v177, v165, v169, vcc quad_perm:[1,0,3,2] row_mask:0xf bank_mask:0xf
	s_mov_b32 vcc_lo, 0x55555555
	s_mov_b32 vcc_hi, 0x55555555
	s_nop 1
	v_cndmask_b32_dpp v154, v158, v154, vcc quad_perm:[1,0,3,2] row_mask:0xf bank_mask:0xf
	v_cndmask_b32_dpp v162, v166, v162, vcc quad_perm:[1,0,3,2] row_mask:0xf bank_mask:0xf
	v_cndmask_b32_dpp v155, v159, v155, vcc quad_perm:[1,0,3,2] row_mask:0xf bank_mask:0xf
	v_cndmask_b32_dpp v163, v167, v163, vcc quad_perm:[1,0,3,2] row_mask:0xf bank_mask:0xf
	v_cndmask_b32_dpp v156, v160, v156, vcc quad_perm:[1,0,3,2] row_mask:0xf bank_mask:0xf
	v_cndmask_b32_dpp v164, v168, v164, vcc quad_perm:[1,0,3,2] row_mask:0xf bank_mask:0xf
	v_cndmask_b32_dpp v157, v161, v157, vcc quad_perm:[1,0,3,2] row_mask:0xf bank_mask:0xf
	v_cndmask_b32_dpp v165, v169, v165, vcc quad_perm:[1,0,3,2] row_mask:0xf bank_mask:0xf
	s_mov_b32 vcc_lo, 0xcccccccc
	s_mov_b32 vcc_hi, 0xcccccccc
	s_nop 1
	v_cndmask_b32_dpp v158, v154, v162, vcc quad_perm:[2,3,0,1] row_mask:0xf bank_mask:0xf
	v_cndmask_b32_dpp v166, v170, v174, vcc quad_perm:[2,3,0,1] row_mask:0xf bank_mask:0xf
	v_cndmask_b32_dpp v159, v155, v163, vcc quad_perm:[2,3,0,1] row_mask:0xf bank_mask:0xf
	v_cndmask_b32_dpp v167, v171, v175, vcc quad_perm:[2,3,0,1] row_mask:0xf bank_mask:0xf
	v_cndmask_b32_dpp v160, v156, v164, vcc quad_perm:[2,3,0,1] row_mask:0xf bank_mask:0xf
	v_cndmask_b32_dpp v168, v172, v176, vcc quad_perm:[2,3,0,1] row_mask:0xf bank_mask:0xf
	v_cndmask_b32_dpp v161, v157, v165, vcc quad_perm:[2,3,0,1] row_mask:0xf bank_mask:0xf
	v_cndmask_b32_dpp v169, v173, v177, vcc quad_perm:[2,3,0,1] row_mask:0xf bank_mask:0xf
	s_mov_b32 vcc_lo, 0x33333333
	s_mov_b32 vcc_hi, 0x33333333
	s_nop 1
	v_cndmask_b32_dpp v154, v162, v154, vcc quad_perm:[2,3,0,1] row_mask:0xf bank_mask:0xf
	v_cndmask_b32_dpp v170, v174, v170, vcc quad_perm:[2,3,0,1] row_mask:0xf bank_mask:0xf
	v_cndmask_b32_dpp v155, v163, v155, vcc quad_perm:[2,3,0,1] row_mask:0xf bank_mask:0xf
	v_cndmask_b32_dpp v171, v175, v171, vcc quad_perm:[2,3,0,1] row_mask:0xf bank_mask:0xf
	v_cndmask_b32_dpp v156, v164, v156, vcc quad_perm:[2,3,0,1] row_mask:0xf bank_mask:0xf
	v_cndmask_b32_dpp v172, v176, v172, vcc quad_perm:[2,3,0,1] row_mask:0xf bank_mask:0xf
	v_cndmask_b32_dpp v157, v165, v157, vcc quad_perm:[2,3,0,1] row_mask:0xf bank_mask:0xf
	v_cndmask_b32_dpp v173, v177, v173, vcc quad_perm:[2,3,0,1] row_mask:0xf bank_mask:0xf
	global_store_dwordx4 v179, v[154:157], s[82:83] sc1
	global_store_dwordx4 v180, v[170:173], s[82:83] sc1
	global_store_dwordx4 v181, v[158:161], s[82:83] sc1
	global_store_dwordx4 v190, v[166:169], s[82:83] sc1
	v_readlane_b32 s2, v239, 0
	s_lshr_b32 s2, s2, 6
	s_add_i32 s2, s2, 6
	s_cmp_gt_u32 s2, 13
	s_cbranch_scc1 .Lhw_seam0_done
	s_add_i32 s2, s2, 0
	s_mul_i32 s2, s2, s74
	v_readlane_b32 s9, v239, 23
	s_lshr_b32 s9, s9, 3
	s_add_i32 s2, s2, s9
	s_cmp_gt_u32 s2, 24575
	s_cbranch_scc1 .Lhw_seam0_done
	v_mbcnt_lo_u32_b32 v178, -1, 0
	v_mbcnt_hi_u32_b32 v178, -1, v178
	v_and_b32_e32 v179, 60, v178
	v_lshlrev_b32_e32 v179, 10, v179
	v_and_b32_e32 v180, 3, v178
	v_lshl_or_b32 v179, v180, 4, v179
	v_add_u32_e32 v180, 0x400, v179
	v_add_u32_e32 v181, 0x800, v179
	v_add_u32_e32 v190, 0xc00, v179
	v_lshlrev_b32_e32 v178, 2, v178
	s_cmp_lt_u32 s2, 16384
	s_cbranch_scc0 .Lhw_dn_s0_1
	s_lshr_b32 s9, s2, 9
	s_bfe_u32 s32, s2, 0x40005
	s_and_b32 s53, s2, 31
	s_lshl_b32 s69, s9, 23
	s_lshl_b32 s100, s32, 19
	s_add_i32 s69, s69, s100
	s_lshl_b32 s100, s53, 8
	s_add_i32 s69, s69, s100
	s_lshl_b32 s98, s9, 11
	s_bfe_u32 s100, s53, 0x30001
	s_lshl_b32 s100, s100, 8
	s_add_i32 s98, s98, s100
	s_lshr_b32 s100, s53, 4
	s_lshl_b32 s100, s100, 7
	s_add_i32 s98, s98, s100
	s_and_b32 s100, s53, 1
	s_lshl_b32 s100, s100, 6
	s_add_i32 s98, s98, s100
	s_lshl_b32 s98, s98, 10
	s_lshl_b32 s100, s32, 6
	s_add_i32 s98, s98, s100
	s_add_i32 s98, s98, 0x2000000
	v_readlane_b32 s82, v239, 11
	v_readlane_b32 s83, v239, 12
	s_movk_i32 s89, 8192
	s_branch .Lhw_go_s0_1

.Lhw_go_s0_1:
	s_add_u32 s100, s82, s69
	s_addc_u32 s101, s83, 0
	v_readlane_b32 s82, v239, 44
	v_readlane_b32 s83, v239, 45
	s_add_u32 s82, s82, s98
	s_addc_u32 s83, s83, 0
	global_load_dword v34, v178, s[100:101] nt
	s_add_u32 s100, s100, s89
	s_addc_u32 s101, s101, 0
	global_load_dword v35, v178, s[100:101] nt
	s_add_u32 s100, s100, s89
	s_addc_u32 s101, s101, 0
	global_load_dword v36, v178, s[100:101] nt
	s_add_u32 s100, s100, s89
	s_addc_u32 s101, s101, 0
	global_load_dword v37, v178, s[100:101] nt
	s_add_u32 s100, s100, s89
	s_addc_u32 s101, s101, 0
	global_load_dword v38, v178, s[100:101] nt
	s_add_u32 s100, s100, s89
	s_addc_u32 s101, s101, 0
	global_load_dword v39, v178, s[100:101] nt
	s_add_u32 s100, s100, s89
	s_addc_u32 s101, s101, 0
	global_load_dword v40, v178, s[100:101] nt
	s_add_u32 s100, s100, s89
	s_addc_u32 s101, s101, 0
	global_load_dword v41, v178, s[100:101] nt
	s_add_u32 s100, s100, s89
	s_addc_u32 s101, s101, 0
	global_load_dword v42, v178, s[100:101] nt
	s_add_u32 s100, s100, s89
	s_addc_u32 s101, s101, 0
	global_load_dword v43, v178, s[100:101] nt
	s_add_u32 s100, s100, s89
	s_addc_u32 s101, s101, 0
	global_load_dword v44, v178, s[100:101] nt
	s_add_u32 s100, s100, s89
	s_addc_u32 s101, s101, 0
	global_load_dword v45, v178, s[100:101] nt
	s_add_u32 s100, s100, s89
	s_addc_u32 s101, s101, 0
	global_load_dword v46, v178, s[100:101] nt
	s_add_u32 s100, s100, s89
	s_addc_u32 s101, s101, 0
	global_load_dword v47, v178, s[100:101] nt
	s_add_u32 s100, s100, s89
	s_addc_u32 s101, s101, 0
	global_load_dword v48, v178, s[100:101] nt
	s_add_u32 s100, s100, s89
	s_addc_u32 s101, s101, 0
	global_load_dword v49, v178, s[100:101] nt
	s_add_u32 s100, s100, s89
	s_addc_u32 s101, s101, 0
	global_load_dword v50, v178, s[100:101] nt
	s_add_u32 s100, s100, s89
	s_addc_u32 s101, s101, 0
	global_load_dword v51, v178, s[100:101] nt
	s_add_u32 s100, s100, s89
	s_addc_u32 s101, s101, 0
	global_load_dword v52, v178, s[100:101] nt
	s_add_u32 s100, s100, s89
	s_addc_u32 s101, s101, 0
	global_load_dword v53, v178, s[100:101] nt
	s_add_u32 s100, s100, s89
	s_addc_u32 s101, s101, 0
	global_load_dword v54, v178, s[100:101] nt
	s_add_u32 s100, s100, s89
	s_addc_u32 s101, s101, 0
	global_load_dword v55, v178, s[100:101] nt
	s_add_u32 s100, s100, s89
	s_addc_u32 s101, s101, 0
	global_load_dword v56, v178, s[100:101] nt
	s_add_u32 s100, s100, s89
	s_addc_u32 s101, s101, 0
	global_load_dword v57, v178, s[100:101] nt
	s_add_u32 s100, s100, s89
	s_addc_u32 s101, s101, 0
	global_load_dword v58, v178, s[100:101] nt
	s_add_u32 s100, s100, s89
	s_addc_u32 s101, s101, 0
	global_load_dword v59, v178, s[100:101] nt
	s_add_u32 s100, s100, s89
	s_addc_u32 s101, s101, 0
	global_load_dword v60, v178, s[100:101] nt
	s_add_u32 s100, s100, s89
	s_addc_u32 s101, s101, 0
	global_load_dword v61, v178, s[100:101] nt
	s_add_u32 s100, s100, s89
	s_addc_u32 s101, s101, 0
	global_load_dword v62, v178, s[100:101] nt
	s_add_u32 s100, s100, s89
	s_addc_u32 s101, s101, 0
	global_load_dword v63, v178, s[100:101] nt
	s_add_u32 s100, s100, s89
	s_addc_u32 s101, s101, 0
	global_load_dword v64, v178, s[100:101] nt
	s_add_u32 s100, s100, s89
	s_addc_u32 s101, s101, 0
	global_load_dword v65, v178, s[100:101] nt
	s_add_u32 s100, s100, s89
	s_addc_u32 s101, s101, 0
	global_load_dword v66, v178, s[100:101] nt
	s_add_u32 s100, s100, s89
	s_addc_u32 s101, s101, 0
	global_load_dword v67, v178, s[100:101] nt
	s_add_u32 s100, s100, s89
	s_addc_u32 s101, s101, 0
	global_load_dword v68, v178, s[100:101] nt
	s_add_u32 s100, s100, s89
	s_addc_u32 s101, s101, 0
	global_load_dword v69, v178, s[100:101] nt
	s_add_u32 s100, s100, s89
	s_addc_u32 s101, s101, 0
	global_load_dword v70, v178, s[100:101] nt
	s_add_u32 s100, s100, s89
	s_addc_u32 s101, s101, 0
	global_load_dword v71, v178, s[100:101] nt
	s_add_u32 s100, s100, s89
	s_addc_u32 s101, s101, 0
	global_load_dword v72, v178, s[100:101] nt
	s_add_u32 s100, s100, s89
	s_addc_u32 s101, s101, 0
	global_load_dword v73, v178, s[100:101] nt
	s_add_u32 s100, s100, s89
	s_addc_u32 s101, s101, 0
	global_load_dword v74, v178, s[100:101] nt
	s_add_u32 s100, s100, s89
	s_addc_u32 s101, s101, 0
	global_load_dword v75, v178, s[100:101] nt
	s_add_u32 s100, s100, s89
	s_addc_u32 s101, s101, 0
	global_load_dword v76, v178, s[100:101] nt
	s_add_u32 s100, s100, s89
	s_addc_u32 s101, s101, 0
	global_load_dword v77, v178, s[100:101] nt
	s_add_u32 s100, s100, s89
	s_addc_u32 s101, s101, 0
	global_load_dword v78, v178, s[100:101] nt
	s_add_u32 s100, s100, s89
	s_addc_u32 s101, s101, 0
	global_load_dword v79, v178, s[100:101] nt
	s_add_u32 s100, s100, s89
	s_addc_u32 s101, s101, 0
	global_load_dword v80, v178, s[100:101] nt
	s_add_u32 s100, s100, s89
	s_addc_u32 s101, s101, 0
	global_load_dword v81, v178, s[100:101] nt
	s_add_u32 s100, s100, s89
	s_addc_u32 s101, s101, 0
	global_load_dword v82, v178, s[100:101] nt
	s_add_u32 s100, s100, s89
	s_addc_u32 s101, s101, 0
	global_load_dword v83, v178, s[100:101] nt
	s_add_u32 s100, s100, s89
	s_addc_u32 s101, s101, 0
	global_load_dword v84, v178, s[100:101] nt
	s_add_u32 s100, s100, s89
	s_addc_u32 s101, s101, 0
	global_load_dword v85, v178, s[100:101] nt
	s_add_u32 s100, s100, s89
	s_addc_u32 s101, s101, 0
	global_load_dword v86, v178, s[100:101] nt
	s_add_u32 s100, s100, s89
	s_addc_u32 s101, s101, 0
	global_load_dword v87, v178, s[100:101] nt
	s_add_u32 s100, s100, s89
	s_addc_u32 s101, s101, 0
	global_load_dword v88, v178, s[100:101] nt
	s_add_u32 s100, s100, s89
	s_addc_u32 s101, s101, 0
	global_load_dword v89, v178, s[100:101] nt
	s_add_u32 s100, s100, s89
	s_addc_u32 s101, s101, 0
	global_load_dword v90, v178, s[100:101] nt
	s_add_u32 s100, s100, s89
	s_addc_u32 s101, s101, 0
	global_load_dword v91, v178, s[100:101] nt
	s_add_u32 s100, s100, s89
	s_addc_u32 s101, s101, 0
	global_load_dword v92, v178, s[100:101] nt
	s_add_u32 s100, s100, s89
	s_addc_u32 s101, s101, 0
	global_load_dword v93, v178, s[100:101] nt
	s_add_u32 s100, s100, s89
	s_addc_u32 s101, s101, 0
	global_load_dword v94, v178, s[100:101] nt
	s_add_u32 s100, s100, s89
	s_addc_u32 s101, s101, 0
	global_load_dword v95, v178, s[100:101] nt
	s_add_u32 s100, s100, s89
	s_addc_u32 s101, s101, 0
	global_load_dword v96, v178, s[100:101] nt
	s_add_u32 s100, s100, s89
	s_addc_u32 s101, s101, 0
	global_load_dword v97, v178, s[100:101] nt
	s_add_u32 s100, s100, s89
	s_addc_u32 s101, s101, 0
	s_waitcnt vmcnt(48)
	v_mul_f32_e32 v34, 0x42000000, v34
	v_mul_f32_e32 v35, 0x42000000, v35
	v_mul_f32_e32 v36, 0x42000000, v36
	v_mul_f32_e32 v37, 0x42000000, v37
	v_mul_f32_e32 v38, 0x42000000, v38
	v_mul_f32_e32 v39, 0x42000000, v39
	v_mul_f32_e32 v40, 0x42000000, v40
	v_mul_f32_e32 v41, 0x42000000, v41
	v_mul_f32_e32 v42, 0x42000000, v42
	v_mul_f32_e32 v43, 0x42000000, v43
	v_mul_f32_e32 v44, 0x42000000, v44
	v_mul_f32_e32 v45, 0x42000000, v45
	v_mul_f32_e32 v46, 0x42000000, v46
	v_mul_f32_e32 v47, 0x42000000, v47
	v_mul_f32_e32 v48, 0x42000000, v48
	v_mul_f32_e32 v49, 0x42000000, v49
	v_cvt_pk_fp8_f32 v154, v34, v35
	v_cvt_pk_fp8_f32 v155, v38, v39
	v_cvt_pk_fp8_f32 v156, v42, v43
	v_cvt_pk_fp8_f32 v157, v46, v47
	v_cvt_pk_fp8_f32 v154, v36, v37 op_sel:[0,0,1]
	v_cvt_pk_fp8_f32 v155, v40, v41 op_sel:[0,0,1]
	v_cvt_pk_fp8_f32 v156, v44, v45 op_sel:[0,0,1]
	v_cvt_pk_fp8_f32 v157, v48, v49 op_sel:[0,0,1]
	s_waitcnt vmcnt(32)
	v_mul_f32_e32 v50, 0x42000000, v50
	v_mul_f32_e32 v51, 0x42000000, v51
	v_mul_f32_e32 v52, 0x42000000, v52
	v_mul_f32_e32 v53, 0x42000000, v53
	v_mul_f32_e32 v54, 0x42000000, v54
	v_mul_f32_e32 v55, 0x42000000, v55
	v_mul_f32_e32 v56, 0x42000000, v56
	v_mul_f32_e32 v57, 0x42000000, v57
	v_mul_f32_e32 v58, 0x42000000, v58
	v_mul_f32_e32 v59, 0x42000000, v59
	v_mul_f32_e32 v60, 0x42000000, v60
	v_mul_f32_e32 v61, 0x42000000, v61
	v_mul_f32_e32 v62, 0x42000000, v62
	v_mul_f32_e32 v63, 0x42000000, v63
	v_mul_f32_e32 v64, 0x42000000, v64
	v_mul_f32_e32 v65, 0x42000000, v65
	v_cvt_pk_fp8_f32 v158, v50, v51
	v_cvt_pk_fp8_f32 v159, v54, v55
	v_cvt_pk_fp8_f32 v160, v58, v59
	v_cvt_pk_fp8_f32 v161, v62, v63
	v_cvt_pk_fp8_f32 v158, v52, v53 op_sel:[0,0,1]
	v_cvt_pk_fp8_f32 v159, v56, v57 op_sel:[0,0,1]
	v_cvt_pk_fp8_f32 v160, v60, v61 op_sel:[0,0,1]
	v_cvt_pk_fp8_f32 v161, v64, v65 op_sel:[0,0,1]
	s_waitcnt vmcnt(16)
	v_mul_f32_e32 v66, 0x42000000, v66
	v_mul_f32_e32 v67, 0x42000000, v67
	v_mul_f32_e32 v68, 0x42000000, v68
	v_mul_f32_e32 v69, 0x42000000, v69
	v_mul_f32_e32 v70, 0x42000000, v70
	v_mul_f32_e32 v71, 0x42000000, v71
	v_mul_f32_e32 v72, 0x42000000, v72
	v_mul_f32_e32 v73, 0x42000000, v73
	v_mul_f32_e32 v74, 0x42000000, v74
	v_mul_f32_e32 v75, 0x42000000, v75
	v_mul_f32_e32 v76, 0x42000000, v76
	v_mul_f32_e32 v77, 0x42000000, v77
	v_mul_f32_e32 v78, 0x42000000, v78
	v_mul_f32_e32 v79, 0x42000000, v79
	v_mul_f32_e32 v80, 0x42000000, v80
	v_mul_f32_e32 v81, 0x42000000, v81
	v_cvt_pk_fp8_f32 v162, v66, v67
	v_cvt_pk_fp8_f32 v163, v70, v71
	v_cvt_pk_fp8_f32 v164, v74, v75
	v_cvt_pk_fp8_f32 v165, v78, v79
	v_cvt_pk_fp8_f32 v162, v68, v69 op_sel:[0,0,1]
	v_cvt_pk_fp8_f32 v163, v72, v73 op_sel:[0,0,1]
	v_cvt_pk_fp8_f32 v164, v76, v77 op_sel:[0,0,1]
	v_cvt_pk_fp8_f32 v165, v80, v81 op_sel:[0,0,1]
	s_waitcnt vmcnt(0)
	v_mul_f32_e32 v82, 0x42000000, v82
	v_mul_f32_e32 v83, 0x42000000, v83
	v_mul_f32_e32 v84, 0x42000000, v84
	v_mul_f32_e32 v85, 0x42000000, v85
	v_mul_f32_e32 v86, 0x42000000, v86
	v_mul_f32_e32 v87, 0x42000000, v87
	v_mul_f32_e32 v88, 0x42000000, v88
	v_mul_f32_e32 v89, 0x42000000, v89
	v_mul_f32_e32 v90, 0x42000000, v90
	v_mul_f32_e32 v91, 0x42000000, v91
	v_mul_f32_e32 v92, 0x42000000, v92
	v_mul_f32_e32 v93, 0x42000000, v93
	v_mul_f32_e32 v94, 0x42000000, v94
	v_mul_f32_e32 v95, 0x42000000, v95
	v_mul_f32_e32 v96, 0x42000000, v96
	v_mul_f32_e32 v97, 0x42000000, v97
	v_cvt_pk_fp8_f32 v166, v82, v83
	v_cvt_pk_fp8_f32 v167, v86, v87
	v_cvt_pk_fp8_f32 v168, v90, v91
	v_cvt_pk_fp8_f32 v169, v94, v95
	v_cvt_pk_fp8_f32 v166, v84, v85 op_sel:[0,0,1]
	v_cvt_pk_fp8_f32 v167, v88, v89 op_sel:[0,0,1]
	v_cvt_pk_fp8_f32 v168, v92, v93 op_sel:[0,0,1]
	v_cvt_pk_fp8_f32 v169, v96, v97 op_sel:[0,0,1]
	s_mov_b32 vcc_lo, 0xaaaaaaaa
	s_mov_b32 vcc_hi, 0xaaaaaaaa
	s_nop 1
	v_cndmask_b32_dpp v170, v154, v158, vcc quad_perm:[1,0,3,2] row_mask:0xf bank_mask:0xf
	v_cndmask_b32_dpp v174, v162, v166, vcc quad_perm:[1,0,3,2] row_mask:0xf bank_mask:0xf
	v_cndmask_b32_dpp v171, v155, v159, vcc quad_perm:[1,0,3,2] row_mask:0xf bank_mask:0xf
	v_cndmask_b32_dpp v175, v163, v167, vcc quad_perm:[1,0,3,2] row_mask:0xf bank_mask:0xf
	v_cndmask_b32_dpp v172, v156, v160, vcc quad_perm:[1,0,3,2] row_mask:0xf bank_mask:0xf
	v_cndmask_b32_dpp v176, v164, v168, vcc quad_perm:[1,0,3,2] row_mask:0xf bank_mask:0xf
	v_cndmask_b32_dpp v173, v157, v161, vcc quad_perm:[1,0,3,2] row_mask:0xf bank_mask:0xf
	v_cndmask_b32_dpp v177, v165, v169, vcc quad_perm:[1,0,3,2] row_mask:0xf bank_mask:0xf
	s_mov_b32 vcc_lo, 0x55555555
	s_mov_b32 vcc_hi, 0x55555555
	s_nop 1
	v_cndmask_b32_dpp v154, v158, v154, vcc quad_perm:[1,0,3,2] row_mask:0xf bank_mask:0xf
	v_cndmask_b32_dpp v162, v166, v162, vcc quad_perm:[1,0,3,2] row_mask:0xf bank_mask:0xf
	v_cndmask_b32_dpp v155, v159, v155, vcc quad_perm:[1,0,3,2] row_mask:0xf bank_mask:0xf
	v_cndmask_b32_dpp v163, v167, v163, vcc quad_perm:[1,0,3,2] row_mask:0xf bank_mask:0xf
	v_cndmask_b32_dpp v156, v160, v156, vcc quad_perm:[1,0,3,2] row_mask:0xf bank_mask:0xf
	v_cndmask_b32_dpp v164, v168, v164, vcc quad_perm:[1,0,3,2] row_mask:0xf bank_mask:0xf
	v_cndmask_b32_dpp v157, v161, v157, vcc quad_perm:[1,0,3,2] row_mask:0xf bank_mask:0xf
	v_cndmask_b32_dpp v165, v169, v165, vcc quad_perm:[1,0,3,2] row_mask:0xf bank_mask:0xf
	s_mov_b32 vcc_lo, 0xcccccccc
	s_mov_b32 vcc_hi, 0xcccccccc
	s_nop 1
	v_cndmask_b32_dpp v158, v154, v162, vcc quad_perm:[2,3,0,1] row_mask:0xf bank_mask:0xf
	v_cndmask_b32_dpp v166, v170, v174, vcc quad_perm:[2,3,0,1] row_mask:0xf bank_mask:0xf
	v_cndmask_b32_dpp v159, v155, v163, vcc quad_perm:[2,3,0,1] row_mask:0xf bank_mask:0xf
	v_cndmask_b32_dpp v167, v171, v175, vcc quad_perm:[2,3,0,1] row_mask:0xf bank_mask:0xf
	v_cndmask_b32_dpp v160, v156, v164, vcc quad_perm:[2,3,0,1] row_mask:0xf bank_mask:0xf
	v_cndmask_b32_dpp v168, v172, v176, vcc quad_perm:[2,3,0,1] row_mask:0xf bank_mask:0xf
	v_cndmask_b32_dpp v161, v157, v165, vcc quad_perm:[2,3,0,1] row_mask:0xf bank_mask:0xf
	v_cndmask_b32_dpp v169, v173, v177, vcc quad_perm:[2,3,0,1] row_mask:0xf bank_mask:0xf
	s_mov_b32 vcc_lo, 0x33333333
	s_mov_b32 vcc_hi, 0x33333333
	s_nop 1
	v_cndmask_b32_dpp v154, v162, v154, vcc quad_perm:[2,3,0,1] row_mask:0xf bank_mask:0xf
	v_cndmask_b32_dpp v170, v174, v170, vcc quad_perm:[2,3,0,1] row_mask:0xf bank_mask:0xf
	v_cndmask_b32_dpp v155, v163, v155, vcc quad_perm:[2,3,0,1] row_mask:0xf bank_mask:0xf
	v_cndmask_b32_dpp v171, v175, v171, vcc quad_perm:[2,3,0,1] row_mask:0xf bank_mask:0xf
	v_cndmask_b32_dpp v156, v164, v156, vcc quad_perm:[2,3,0,1] row_mask:0xf bank_mask:0xf
	v_cndmask_b32_dpp v172, v176, v172, vcc quad_perm:[2,3,0,1] row_mask:0xf bank_mask:0xf
	v_cndmask_b32_dpp v157, v165, v157, vcc quad_perm:[2,3,0,1] row_mask:0xf bank_mask:0xf
	v_cndmask_b32_dpp v173, v177, v173, vcc quad_perm:[2,3,0,1] row_mask:0xf bank_mask:0xf
	global_store_dwordx4 v179, v[154:157], s[82:83] sc1
	global_store_dwordx4 v180, v[170:173], s[82:83] sc1
	global_store_dwordx4 v181, v[158:161], s[82:83] sc1
	global_store_dwordx4 v190, v[166:169], s[82:83] sc1

.Lhw_go_s1_0:
	s_add_u32 s100, s82, s69
	s_addc_u32 s101, s83, 0
	v_readlane_b32 s82, v239, 44
	v_readlane_b32 s83, v239, 45
	s_add_u32 s82, s82, s98
	s_addc_u32 s83, s83, 0
	global_load_dword v34, v178, s[100:101] nt
	s_add_u32 s100, s100, s89
	s_addc_u32 s101, s101, 0
	global_load_dword v35, v178, s[100:101] nt
	s_add_u32 s100, s100, s89
	s_addc_u32 s101, s101, 0
	global_load_dword v36, v178, s[100:101] nt
	s_add_u32 s100, s100, s89
	s_addc_u32 s101, s101, 0
	global_load_dword v37, v178, s[100:101] nt
	s_add_u32 s100, s100, s89
	s_addc_u32 s101, s101, 0
	global_load_dword v38, v178, s[100:101] nt
	s_add_u32 s100, s100, s89
	s_addc_u32 s101, s101, 0
	global_load_dword v39, v178, s[100:101] nt
	s_add_u32 s100, s100, s89
	s_addc_u32 s101, s101, 0
	global_load_dword v40, v178, s[100:101] nt
	s_add_u32 s100, s100, s89
	s_addc_u32 s101, s101, 0
	global_load_dword v41, v178, s[100:101] nt
	s_add_u32 s100, s100, s89
	s_addc_u32 s101, s101, 0
	global_load_dword v42, v178, s[100:101] nt
	s_add_u32 s100, s100, s89
	s_addc_u32 s101, s101, 0
	global_load_dword v43, v178, s[100:101] nt
	s_add_u32 s100, s100, s89
	s_addc_u32 s101, s101, 0
	global_load_dword v44, v178, s[100:101] nt
	s_add_u32 s100, s100, s89
	s_addc_u32 s101, s101, 0
	global_load_dword v45, v178, s[100:101] nt
	s_add_u32 s100, s100, s89
	s_addc_u32 s101, s101, 0
	global_load_dword v46, v178, s[100:101] nt
	s_add_u32 s100, s100, s89
	s_addc_u32 s101, s101, 0
	global_load_dword v47, v178, s[100:101] nt
	s_add_u32 s100, s100, s89
	s_addc_u32 s101, s101, 0
	global_load_dword v48, v178, s[100:101] nt
	s_add_u32 s100, s100, s89
	s_addc_u32 s101, s101, 0
	global_load_dword v49, v178, s[100:101] nt
	s_add_u32 s100, s100, s89
	s_addc_u32 s101, s101, 0
	global_load_dword v50, v178, s[100:101] nt
	s_add_u32 s100, s100, s89
	s_addc_u32 s101, s101, 0
	global_load_dword v51, v178, s[100:101] nt
	s_add_u32 s100, s100, s89
	s_addc_u32 s101, s101, 0
	global_load_dword v52, v178, s[100:101] nt
	s_add_u32 s100, s100, s89
	s_addc_u32 s101, s101, 0
	global_load_dword v53, v178, s[100:101] nt
	s_add_u32 s100, s100, s89
	s_addc_u32 s101, s101, 0
	global_load_dword v54, v178, s[100:101] nt
	s_add_u32 s100, s100, s89
	s_addc_u32 s101, s101, 0
	global_load_dword v55, v178, s[100:101] nt
	s_add_u32 s100, s100, s89
	s_addc_u32 s101, s101, 0
	global_load_dword v56, v178, s[100:101] nt
	s_add_u32 s100, s100, s89
	s_addc_u32 s101, s101, 0
	global_load_dword v57, v178, s[100:101] nt
	s_add_u32 s100, s100, s89
	s_addc_u32 s101, s101, 0
	global_load_dword v58, v178, s[100:101] nt
	s_add_u32 s100, s100, s89
	s_addc_u32 s101, s101, 0
	global_load_dword v59, v178, s[100:101] nt
	s_add_u32 s100, s100, s89
	s_addc_u32 s101, s101, 0
	global_load_dword v60, v178, s[100:101] nt
	s_add_u32 s100, s100, s89
	s_addc_u32 s101, s101, 0
	global_load_dword v61, v178, s[100:101] nt
	s_add_u32 s100, s100, s89
	s_addc_u32 s101, s101, 0
	global_load_dword v62, v178, s[100:101] nt
	s_add_u32 s100, s100, s89
	s_addc_u32 s101, s101, 0
	global_load_dword v63, v178, s[100:101] nt
	s_add_u32 s100, s100, s89
	s_addc_u32 s101, s101, 0
	global_load_dword v64, v178, s[100:101] nt
	s_add_u32 s100, s100, s89
	s_addc_u32 s101, s101, 0
	global_load_dword v65, v178, s[100:101] nt
	s_add_u32 s100, s100, s89
	s_addc_u32 s101, s101, 0
	global_load_dword v66, v178, s[100:101] nt
	s_add_u32 s100, s100, s89
	s_addc_u32 s101, s101, 0
	global_load_dword v67, v178, s[100:101] nt
	s_add_u32 s100, s100, s89
	s_addc_u32 s101, s101, 0
	global_load_dword v68, v178, s[100:101] nt
	s_add_u32 s100, s100, s89
	s_addc_u32 s101, s101, 0
	global_load_dword v69, v178, s[100:101] nt
	s_add_u32 s100, s100, s89
	s_addc_u32 s101, s101, 0
	global_load_dword v70, v178, s[100:101] nt
	s_add_u32 s100, s100, s89
	s_addc_u32 s101, s101, 0
	global_load_dword v71, v178, s[100:101] nt
	s_add_u32 s100, s100, s89
	s_addc_u32 s101, s101, 0
	global_load_dword v72, v178, s[100:101] nt
	s_add_u32 s100, s100, s89
	s_addc_u32 s101, s101, 0
	global_load_dword v73, v178, s[100:101] nt
	s_add_u32 s100, s100, s89
	s_addc_u32 s101, s101, 0
	global_load_dword v74, v178, s[100:101] nt
	s_add_u32 s100, s100, s89
	s_addc_u32 s101, s101, 0
	global_load_dword v75, v178, s[100:101] nt
	s_add_u32 s100, s100, s89
	s_addc_u32 s101, s101, 0
	global_load_dword v76, v178, s[100:101] nt
	s_add_u32 s100, s100, s89
	s_addc_u32 s101, s101, 0
	global_load_dword v77, v178, s[100:101] nt
	s_add_u32 s100, s100, s89
	s_addc_u32 s101, s101, 0
	global_load_dword v78, v178, s[100:101] nt
	s_add_u32 s100, s100, s89
	s_addc_u32 s101, s101, 0
	global_load_dword v79, v178, s[100:101] nt
	s_add_u32 s100, s100, s89
	s_addc_u32 s101, s101, 0
	global_load_dword v80, v178, s[100:101] nt
	s_add_u32 s100, s100, s89
	s_addc_u32 s101, s101, 0
	global_load_dword v81, v178, s[100:101] nt
	s_add_u32 s100, s100, s89
	s_addc_u32 s101, s101, 0
	global_load_dword v82, v178, s[100:101] nt
	s_add_u32 s100, s100, s89
	s_addc_u32 s101, s101, 0
	global_load_dword v83, v178, s[100:101] nt
	s_add_u32 s100, s100, s89
	s_addc_u32 s101, s101, 0
	global_load_dword v84, v178, s[100:101] nt
	s_add_u32 s100, s100, s89
	s_addc_u32 s101, s101, 0
	global_load_dword v85, v178, s[100:101] nt
	s_add_u32 s100, s100, s89
	s_addc_u32 s101, s101, 0
	global_load_dword v86, v178, s[100:101] nt
	s_add_u32 s100, s100, s89
	s_addc_u32 s101, s101, 0
	global_load_dword v87, v178, s[100:101] nt
	s_add_u32 s100, s100, s89
	s_addc_u32 s101, s101, 0
	global_load_dword v88, v178, s[100:101] nt
	s_add_u32 s100, s100, s89
	s_addc_u32 s101, s101, 0
	global_load_dword v89, v178, s[100:101] nt
	s_add_u32 s100, s100, s89
	s_addc_u32 s101, s101, 0
	global_load_dword v90, v178, s[100:101] nt
	s_add_u32 s100, s100, s89
	s_addc_u32 s101, s101, 0
	global_load_dword v91, v178, s[100:101] nt
	s_add_u32 s100, s100, s89
	s_addc_u32 s101, s101, 0
	global_load_dword v92, v178, s[100:101] nt
	s_add_u32 s100, s100, s89
	s_addc_u32 s101, s101, 0
	global_load_dword v93, v178, s[100:101] nt
	s_add_u32 s100, s100, s89
	s_addc_u32 s101, s101, 0
	global_load_dword v94, v178, s[100:101] nt
	s_add_u32 s100, s100, s89
	s_addc_u32 s101, s101, 0
	global_load_dword v95, v178, s[100:101] nt
	s_add_u32 s100, s100, s89
	s_addc_u32 s101, s101, 0
	global_load_dword v96, v178, s[100:101] nt
	s_add_u32 s100, s100, s89
	s_addc_u32 s101, s101, 0
	global_load_dword v97, v178, s[100:101] nt
	s_add_u32 s100, s100, s89
	s_addc_u32 s101, s101, 0
	s_waitcnt vmcnt(48)
	v_mul_f32_e32 v34, 0x42000000, v34
	v_mul_f32_e32 v35, 0x42000000, v35
	v_mul_f32_e32 v36, 0x42000000, v36
	v_mul_f32_e32 v37, 0x42000000, v37
	v_mul_f32_e32 v38, 0x42000000, v38
	v_mul_f32_e32 v39, 0x42000000, v39
	v_mul_f32_e32 v40, 0x42000000, v40
	v_mul_f32_e32 v41, 0x42000000, v41
	v_mul_f32_e32 v42, 0x42000000, v42
	v_mul_f32_e32 v43, 0x42000000, v43
	v_mul_f32_e32 v44, 0x42000000, v44
	v_mul_f32_e32 v45, 0x42000000, v45
	v_mul_f32_e32 v46, 0x42000000, v46
	v_mul_f32_e32 v47, 0x42000000, v47
	v_mul_f32_e32 v48, 0x42000000, v48
	v_mul_f32_e32 v49, 0x42000000, v49
	v_cvt_pk_fp8_f32 v154, v34, v35
	v_cvt_pk_fp8_f32 v155, v38, v39
	v_cvt_pk_fp8_f32 v156, v42, v43
	v_cvt_pk_fp8_f32 v157, v46, v47
	v_cvt_pk_fp8_f32 v154, v36, v37 op_sel:[0,0,1]
	v_cvt_pk_fp8_f32 v155, v40, v41 op_sel:[0,0,1]
	v_cvt_pk_fp8_f32 v156, v44, v45 op_sel:[0,0,1]
	v_cvt_pk_fp8_f32 v157, v48, v49 op_sel:[0,0,1]
	s_waitcnt vmcnt(32)
	v_mul_f32_e32 v50, 0x42000000, v50
	v_mul_f32_e32 v51, 0x42000000, v51
	v_mul_f32_e32 v52, 0x42000000, v52
	v_mul_f32_e32 v53, 0x42000000, v53
	v_mul_f32_e32 v54, 0x42000000, v54
	v_mul_f32_e32 v55, 0x42000000, v55
	v_mul_f32_e32 v56, 0x42000000, v56
	v_mul_f32_e32 v57, 0x42000000, v57
	v_mul_f32_e32 v58, 0x42000000, v58
	v_mul_f32_e32 v59, 0x42000000, v59
	v_mul_f32_e32 v60, 0x42000000, v60
	v_mul_f32_e32 v61, 0x42000000, v61
	v_mul_f32_e32 v62, 0x42000000, v62
	v_mul_f32_e32 v63, 0x42000000, v63
	v_mul_f32_e32 v64, 0x42000000, v64
	v_mul_f32_e32 v65, 0x42000000, v65
	v_cvt_pk_fp8_f32 v158, v50, v51
	v_cvt_pk_fp8_f32 v159, v54, v55
	v_cvt_pk_fp8_f32 v160, v58, v59
	v_cvt_pk_fp8_f32 v161, v62, v63
	v_cvt_pk_fp8_f32 v158, v52, v53 op_sel:[0,0,1]
	v_cvt_pk_fp8_f32 v159, v56, v57 op_sel:[0,0,1]
	v_cvt_pk_fp8_f32 v160, v60, v61 op_sel:[0,0,1]
	v_cvt_pk_fp8_f32 v161, v64, v65 op_sel:[0,0,1]
	s_waitcnt vmcnt(16)
	v_mul_f32_e32 v66, 0x42000000, v66
	v_mul_f32_e32 v67, 0x42000000, v67
	v_mul_f32_e32 v68, 0x42000000, v68
	v_mul_f32_e32 v69, 0x42000000, v69
	v_mul_f32_e32 v70, 0x42000000, v70
	v_mul_f32_e32 v71, 0x42000000, v71
	v_mul_f32_e32 v72, 0x42000000, v72
	v_mul_f32_e32 v73, 0x42000000, v73
	v_mul_f32_e32 v74, 0x42000000, v74
	v_mul_f32_e32 v75, 0x42000000, v75
	v_mul_f32_e32 v76, 0x42000000, v76
	v_mul_f32_e32 v77, 0x42000000, v77
	v_mul_f32_e32 v78, 0x42000000, v78
	v_mul_f32_e32 v79, 0x42000000, v79
	v_mul_f32_e32 v80, 0x42000000, v80
	v_mul_f32_e32 v81, 0x42000000, v81
	v_cvt_pk_fp8_f32 v162, v66, v67
	v_cvt_pk_fp8_f32 v163, v70, v71
	v_cvt_pk_fp8_f32 v164, v74, v75
	v_cvt_pk_fp8_f32 v165, v78, v79
	v_cvt_pk_fp8_f32 v162, v68, v69 op_sel:[0,0,1]
	v_cvt_pk_fp8_f32 v163, v72, v73 op_sel:[0,0,1]
	v_cvt_pk_fp8_f32 v164, v76, v77 op_sel:[0,0,1]
	v_cvt_pk_fp8_f32 v165, v80, v81 op_sel:[0,0,1]
	s_waitcnt vmcnt(0)
	v_mul_f32_e32 v82, 0x42000000, v82
	v_mul_f32_e32 v83, 0x42000000, v83
	v_mul_f32_e32 v84, 0x42000000, v84
	v_mul_f32_e32 v85, 0x42000000, v85
	v_mul_f32_e32 v86, 0x42000000, v86
	v_mul_f32_e32 v87, 0x42000000, v87
	v_mul_f32_e32 v88, 0x42000000, v88
	v_mul_f32_e32 v89, 0x42000000, v89
	v_mul_f32_e32 v90, 0x42000000, v90
	v_mul_f32_e32 v91, 0x42000000, v91
	v_mul_f32_e32 v92, 0x42000000, v92
	v_mul_f32_e32 v93, 0x42000000, v93
	v_mul_f32_e32 v94, 0x42000000, v94
	v_mul_f32_e32 v95, 0x42000000, v95
	v_mul_f32_e32 v96, 0x42000000, v96
	v_mul_f32_e32 v97, 0x42000000, v97
	v_cvt_pk_fp8_f32 v166, v82, v83
	v_cvt_pk_fp8_f32 v167, v86, v87
	v_cvt_pk_fp8_f32 v168, v90, v91
	v_cvt_pk_fp8_f32 v169, v94, v95
	v_cvt_pk_fp8_f32 v166, v84, v85 op_sel:[0,0,1]
	v_cvt_pk_fp8_f32 v167, v88, v89 op_sel:[0,0,1]
	v_cvt_pk_fp8_f32 v168, v92, v93 op_sel:[0,0,1]
	v_cvt_pk_fp8_f32 v169, v96, v97 op_sel:[0,0,1]
	s_mov_b32 vcc_lo, 0xaaaaaaaa
	s_mov_b32 vcc_hi, 0xaaaaaaaa
	s_nop 1
	v_cndmask_b32_dpp v170, v154, v158, vcc quad_perm:[1,0,3,2] row_mask:0xf bank_mask:0xf
	v_cndmask_b32_dpp v174, v162, v166, vcc quad_perm:[1,0,3,2] row_mask:0xf bank_mask:0xf
	v_cndmask_b32_dpp v171, v155, v159, vcc quad_perm:[1,0,3,2] row_mask:0xf bank_mask:0xf
	v_cndmask_b32_dpp v175, v163, v167, vcc quad_perm:[1,0,3,2] row_mask:0xf bank_mask:0xf
	v_cndmask_b32_dpp v172, v156, v160, vcc quad_perm:[1,0,3,2] row_mask:0xf bank_mask:0xf
	v_cndmask_b32_dpp v176, v164, v168, vcc quad_perm:[1,0,3,2] row_mask:0xf bank_mask:0xf
	v_cndmask_b32_dpp v173, v157, v161, vcc quad_perm:[1,0,3,2] row_mask:0xf bank_mask:0xf
	v_cndmask_b32_dpp v177, v165, v169, vcc quad_perm:[1,0,3,2] row_mask:0xf bank_mask:0xf
	s_mov_b32 vcc_lo, 0x55555555
	s_mov_b32 vcc_hi, 0x55555555
	s_nop 1
	v_cndmask_b32_dpp v154, v158, v154, vcc quad_perm:[1,0,3,2] row_mask:0xf bank_mask:0xf
	v_cndmask_b32_dpp v162, v166, v162, vcc quad_perm:[1,0,3,2] row_mask:0xf bank_mask:0xf
	v_cndmask_b32_dpp v155, v159, v155, vcc quad_perm:[1,0,3,2] row_mask:0xf bank_mask:0xf
	v_cndmask_b32_dpp v163, v167, v163, vcc quad_perm:[1,0,3,2] row_mask:0xf bank_mask:0xf
	v_cndmask_b32_dpp v156, v160, v156, vcc quad_perm:[1,0,3,2] row_mask:0xf bank_mask:0xf
	v_cndmask_b32_dpp v164, v168, v164, vcc quad_perm:[1,0,3,2] row_mask:0xf bank_mask:0xf
	v_cndmask_b32_dpp v157, v161, v157, vcc quad_perm:[1,0,3,2] row_mask:0xf bank_mask:0xf
	v_cndmask_b32_dpp v165, v169, v165, vcc quad_perm:[1,0,3,2] row_mask:0xf bank_mask:0xf
	s_mov_b32 vcc_lo, 0xcccccccc
	s_mov_b32 vcc_hi, 0xcccccccc
	s_nop 1
	v_cndmask_b32_dpp v158, v154, v162, vcc quad_perm:[2,3,0,1] row_mask:0xf bank_mask:0xf
	v_cndmask_b32_dpp v166, v170, v174, vcc quad_perm:[2,3,0,1] row_mask:0xf bank_mask:0xf
	v_cndmask_b32_dpp v159, v155, v163, vcc quad_perm:[2,3,0,1] row_mask:0xf bank_mask:0xf
	v_cndmask_b32_dpp v167, v171, v175, vcc quad_perm:[2,3,0,1] row_mask:0xf bank_mask:0xf
	v_cndmask_b32_dpp v160, v156, v164, vcc quad_perm:[2,3,0,1] row_mask:0xf bank_mask:0xf
	v_cndmask_b32_dpp v168, v172, v176, vcc quad_perm:[2,3,0,1] row_mask:0xf bank_mask:0xf
	v_cndmask_b32_dpp v161, v157, v165, vcc quad_perm:[2,3,0,1] row_mask:0xf bank_mask:0xf
	v_cndmask_b32_dpp v169, v173, v177, vcc quad_perm:[2,3,0,1] row_mask:0xf bank_mask:0xf
	s_mov_b32 vcc_lo, 0x33333333
	s_mov_b32 vcc_hi, 0x33333333
	s_nop 1
	v_cndmask_b32_dpp v154, v162, v154, vcc quad_perm:[2,3,0,1] row_mask:0xf bank_mask:0xf
	v_cndmask_b32_dpp v170, v174, v170, vcc quad_perm:[2,3,0,1] row_mask:0xf bank_mask:0xf
	v_cndmask_b32_dpp v155, v163, v155, vcc quad_perm:[2,3,0,1] row_mask:0xf bank_mask:0xf
	v_cndmask_b32_dpp v171, v175, v171, vcc quad_perm:[2,3,0,1] row_mask:0xf bank_mask:0xf
	v_cndmask_b32_dpp v156, v164, v156, vcc quad_perm:[2,3,0,1] row_mask:0xf bank_mask:0xf
	v_cndmask_b32_dpp v172, v176, v172, vcc quad_perm:[2,3,0,1] row_mask:0xf bank_mask:0xf
	v_cndmask_b32_dpp v157, v165, v157, vcc quad_perm:[2,3,0,1] row_mask:0xf bank_mask:0xf
	v_cndmask_b32_dpp v173, v177, v173, vcc quad_perm:[2,3,0,1] row_mask:0xf bank_mask:0xf
	global_store_dwordx4 v179, v[154:157], s[82:83] sc1
	global_store_dwordx4 v180, v[170:173], s[82:83] sc1
	global_store_dwordx4 v181, v[158:161], s[82:83] sc1
	global_store_dwordx4 v190, v[166:169], s[82:83] sc1
	v_readlane_b32 s2, v239, 0
	s_lshr_b32 s2, s2, 6
	s_add_i32 s2, s2, 6
	s_cmp_gt_u32 s2, 13
	s_cbranch_scc1 .Lhw_seam1_done
	s_add_i32 s2, s2, 14
	s_mul_i32 s2, s2, s74
	v_readlane_b32 s9, v239, 23
	s_lshr_b32 s9, s9, 3
	s_add_i32 s2, s2, s9
	s_cmp_gt_u32 s2, 24575
	s_cbranch_scc1 .Lhw_seam1_done
	v_mbcnt_lo_u32_b32 v178, -1, 0
	v_mbcnt_hi_u32_b32 v178, -1, v178
	v_and_b32_e32 v179, 60, v178
	v_lshlrev_b32_e32 v179, 10, v179
	v_and_b32_e32 v180, 3, v178
	v_lshl_or_b32 v179, v180, 4, v179
	v_add_u32_e32 v180, 0x400, v179
	v_add_u32_e32 v181, 0x800, v179
	v_add_u32_e32 v190, 0xc00, v179
	v_lshlrev_b32_e32 v178, 2, v178
	s_cmp_lt_u32 s2, 16384
	s_cbranch_scc0 .Lhw_dn_s1_1
	s_lshr_b32 s9, s2, 9
	s_bfe_u32 s32, s2, 0x40005
	s_and_b32 s53, s2, 31
	s_lshl_b32 s69, s9, 23
	s_lshl_b32 s100, s32, 19
	s_add_i32 s69, s69, s100
	s_lshl_b32 s100, s53, 8
	s_add_i32 s69, s69, s100
	s_lshl_b32 s98, s9, 11
	s_bfe_u32 s100, s53, 0x30001
	s_lshl_b32 s100, s100, 8
	s_add_i32 s98, s98, s100
	s_lshr_b32 s100, s53, 4
	s_lshl_b32 s100, s100, 7
	s_add_i32 s98, s98, s100
	s_and_b32 s100, s53, 1
	s_lshl_b32 s100, s100, 6
	s_add_i32 s98, s98, s100
	s_lshl_b32 s98, s98, 10
	s_lshl_b32 s100, s32, 6
	s_add_i32 s98, s98, s100
	s_add_i32 s98, s98, 0x2000000
	v_readlane_b32 s82, v239, 11
	v_readlane_b32 s83, v239, 12
	s_movk_i32 s89, 8192
	s_branch .Lhw_go_s1_1

.Lhw_go_s2_0:
	s_add_u32 s100, s82, s69
	s_addc_u32 s101, s83, 0
	v_readlane_b32 s82, v239, 44
	v_readlane_b32 s83, v239, 45
	s_add_u32 s82, s82, s98
	s_addc_u32 s83, s83, 0
	global_load_dword v34, v178, s[100:101] nt
	s_add_u32 s100, s100, s89
	s_addc_u32 s101, s101, 0
	global_load_dword v35, v178, s[100:101] nt
	s_add_u32 s100, s100, s89
	s_addc_u32 s101, s101, 0
	global_load_dword v36, v178, s[100:101] nt
	s_add_u32 s100, s100, s89
	s_addc_u32 s101, s101, 0
	global_load_dword v37, v178, s[100:101] nt
	s_add_u32 s100, s100, s89
	s_addc_u32 s101, s101, 0
	global_load_dword v38, v178, s[100:101] nt
	s_add_u32 s100, s100, s89
	s_addc_u32 s101, s101, 0
	global_load_dword v39, v178, s[100:101] nt
	s_add_u32 s100, s100, s89
	s_addc_u32 s101, s101, 0
	global_load_dword v40, v178, s[100:101] nt
	s_add_u32 s100, s100, s89
	s_addc_u32 s101, s101, 0
	global_load_dword v41, v178, s[100:101] nt
	s_add_u32 s100, s100, s89
	s_addc_u32 s101, s101, 0
	global_load_dword v42, v178, s[100:101] nt
	s_add_u32 s100, s100, s89
	s_addc_u32 s101, s101, 0
	global_load_dword v43, v178, s[100:101] nt
	s_add_u32 s100, s100, s89
	s_addc_u32 s101, s101, 0
	global_load_dword v44, v178, s[100:101] nt
	s_add_u32 s100, s100, s89
	s_addc_u32 s101, s101, 0
	global_load_dword v45, v178, s[100:101] nt
	s_add_u32 s100, s100, s89
	s_addc_u32 s101, s101, 0
	global_load_dword v46, v178, s[100:101] nt
	s_add_u32 s100, s100, s89
	s_addc_u32 s101, s101, 0
	global_load_dword v47, v178, s[100:101] nt
	s_add_u32 s100, s100, s89
	s_addc_u32 s101, s101, 0
	global_load_dword v48, v178, s[100:101] nt
	s_add_u32 s100, s100, s89
	s_addc_u32 s101, s101, 0
	global_load_dword v49, v178, s[100:101] nt
	s_add_u32 s100, s100, s89
	s_addc_u32 s101, s101, 0
	global_load_dword v50, v178, s[100:101] nt
	s_add_u32 s100, s100, s89
	s_addc_u32 s101, s101, 0
	global_load_dword v51, v178, s[100:101] nt
	s_add_u32 s100, s100, s89
	s_addc_u32 s101, s101, 0
	global_load_dword v52, v178, s[100:101] nt
	s_add_u32 s100, s100, s89
	s_addc_u32 s101, s101, 0
	global_load_dword v53, v178, s[100:101] nt
	s_add_u32 s100, s100, s89
	s_addc_u32 s101, s101, 0
	global_load_dword v54, v178, s[100:101] nt
	s_add_u32 s100, s100, s89
	s_addc_u32 s101, s101, 0
	global_load_dword v55, v178, s[100:101] nt
	s_add_u32 s100, s100, s89
	s_addc_u32 s101, s101, 0
	global_load_dword v56, v178, s[100:101] nt
	s_add_u32 s100, s100, s89
	s_addc_u32 s101, s101, 0
	global_load_dword v57, v178, s[100:101] nt
	s_add_u32 s100, s100, s89
	s_addc_u32 s101, s101, 0
	global_load_dword v58, v178, s[100:101] nt
	s_add_u32 s100, s100, s89
	s_addc_u32 s101, s101, 0
	global_load_dword v59, v178, s[100:101] nt
	s_add_u32 s100, s100, s89
	s_addc_u32 s101, s101, 0
	global_load_dword v60, v178, s[100:101] nt
	s_add_u32 s100, s100, s89
	s_addc_u32 s101, s101, 0
	global_load_dword v61, v178, s[100:101] nt
	s_add_u32 s100, s100, s89
	s_addc_u32 s101, s101, 0
	global_load_dword v62, v178, s[100:101] nt
	s_add_u32 s100, s100, s89
	s_addc_u32 s101, s101, 0
	global_load_dword v63, v178, s[100:101] nt
	s_add_u32 s100, s100, s89
	s_addc_u32 s101, s101, 0
	global_load_dword v64, v178, s[100:101] nt
	s_add_u32 s100, s100, s89
	s_addc_u32 s101, s101, 0
	global_load_dword v65, v178, s[100:101] nt
	s_add_u32 s100, s100, s89
	s_addc_u32 s101, s101, 0
	global_load_dword v66, v178, s[100:101] nt
	s_add_u32 s100, s100, s89
	s_addc_u32 s101, s101, 0
	global_load_dword v67, v178, s[100:101] nt
	s_add_u32 s100, s100, s89
	s_addc_u32 s101, s101, 0
	global_load_dword v68, v178, s[100:101] nt
	s_add_u32 s100, s100, s89
	s_addc_u32 s101, s101, 0
	global_load_dword v69, v178, s[100:101] nt
	s_add_u32 s100, s100, s89
	s_addc_u32 s101, s101, 0
	global_load_dword v70, v178, s[100:101] nt
	s_add_u32 s100, s100, s89
	s_addc_u32 s101, s101, 0
	global_load_dword v71, v178, s[100:101] nt
	s_add_u32 s100, s100, s89
	s_addc_u32 s101, s101, 0
	global_load_dword v72, v178, s[100:101] nt
	s_add_u32 s100, s100, s89
	s_addc_u32 s101, s101, 0
	global_load_dword v73, v178, s[100:101] nt
	s_add_u32 s100, s100, s89
	s_addc_u32 s101, s101, 0
	global_load_dword v74, v178, s[100:101] nt
	s_add_u32 s100, s100, s89
	s_addc_u32 s101, s101, 0
	global_load_dword v75, v178, s[100:101] nt
	s_add_u32 s100, s100, s89
	s_addc_u32 s101, s101, 0
	global_load_dword v76, v178, s[100:101] nt
	s_add_u32 s100, s100, s89
	s_addc_u32 s101, s101, 0
	global_load_dword v77, v178, s[100:101] nt
	s_add_u32 s100, s100, s89
	s_addc_u32 s101, s101, 0
	global_load_dword v78, v178, s[100:101] nt
	s_add_u32 s100, s100, s89
	s_addc_u32 s101, s101, 0
	global_load_dword v79, v178, s[100:101] nt
	s_add_u32 s100, s100, s89
	s_addc_u32 s101, s101, 0
	global_load_dword v80, v178, s[100:101] nt
	s_add_u32 s100, s100, s89
	s_addc_u32 s101, s101, 0
	global_load_dword v81, v178, s[100:101] nt
	s_add_u32 s100, s100, s89
	s_addc_u32 s101, s101, 0
	global_load_dword v82, v178, s[100:101] nt
	s_add_u32 s100, s100, s89
	s_addc_u32 s101, s101, 0
	global_load_dword v83, v178, s[100:101] nt
	s_add_u32 s100, s100, s89
	s_addc_u32 s101, s101, 0
	global_load_dword v84, v178, s[100:101] nt
	s_add_u32 s100, s100, s89
	s_addc_u32 s101, s101, 0
	global_load_dword v85, v178, s[100:101] nt
	s_add_u32 s100, s100, s89
	s_addc_u32 s101, s101, 0
	global_load_dword v86, v178, s[100:101] nt
	s_add_u32 s100, s100, s89
	s_addc_u32 s101, s101, 0
	global_load_dword v87, v178, s[100:101] nt
	s_add_u32 s100, s100, s89
	s_addc_u32 s101, s101, 0
	global_load_dword v88, v178, s[100:101] nt
	s_add_u32 s100, s100, s89
	s_addc_u32 s101, s101, 0
	global_load_dword v89, v178, s[100:101] nt
	s_add_u32 s100, s100, s89
	s_addc_u32 s101, s101, 0
	global_load_dword v90, v178, s[100:101] nt
	s_add_u32 s100, s100, s89
	s_addc_u32 s101, s101, 0
	global_load_dword v91, v178, s[100:101] nt
	s_add_u32 s100, s100, s89
	s_addc_u32 s101, s101, 0
	global_load_dword v92, v178, s[100:101] nt
	s_add_u32 s100, s100, s89
	s_addc_u32 s101, s101, 0
	global_load_dword v93, v178, s[100:101] nt
	s_add_u32 s100, s100, s89
	s_addc_u32 s101, s101, 0
	global_load_dword v94, v178, s[100:101] nt
	s_add_u32 s100, s100, s89
	s_addc_u32 s101, s101, 0
	global_load_dword v95, v178, s[100:101] nt
	s_add_u32 s100, s100, s89
	s_addc_u32 s101, s101, 0
	global_load_dword v96, v178, s[100:101] nt
	s_add_u32 s100, s100, s89
	s_addc_u32 s101, s101, 0
	global_load_dword v97, v178, s[100:101] nt
	s_add_u32 s100, s100, s89
	s_addc_u32 s101, s101, 0
	s_waitcnt vmcnt(48)
	v_mul_f32_e32 v34, 0x42000000, v34
	v_mul_f32_e32 v35, 0x42000000, v35
	v_mul_f32_e32 v36, 0x42000000, v36
	v_mul_f32_e32 v37, 0x42000000, v37
	v_mul_f32_e32 v38, 0x42000000, v38
	v_mul_f32_e32 v39, 0x42000000, v39
	v_mul_f32_e32 v40, 0x42000000, v40
	v_mul_f32_e32 v41, 0x42000000, v41
	v_mul_f32_e32 v42, 0x42000000, v42
	v_mul_f32_e32 v43, 0x42000000, v43
	v_mul_f32_e32 v44, 0x42000000, v44
	v_mul_f32_e32 v45, 0x42000000, v45
	v_mul_f32_e32 v46, 0x42000000, v46
	v_mul_f32_e32 v47, 0x42000000, v47
	v_mul_f32_e32 v48, 0x42000000, v48
	v_mul_f32_e32 v49, 0x42000000, v49
	v_cvt_pk_fp8_f32 v154, v34, v35
	v_cvt_pk_fp8_f32 v155, v38, v39
	v_cvt_pk_fp8_f32 v156, v42, v43
	v_cvt_pk_fp8_f32 v157, v46, v47
	v_cvt_pk_fp8_f32 v154, v36, v37 op_sel:[0,0,1]
	v_cvt_pk_fp8_f32 v155, v40, v41 op_sel:[0,0,1]
	v_cvt_pk_fp8_f32 v156, v44, v45 op_sel:[0,0,1]
	v_cvt_pk_fp8_f32 v157, v48, v49 op_sel:[0,0,1]
	s_waitcnt vmcnt(32)
	v_mul_f32_e32 v50, 0x42000000, v50
	v_mul_f32_e32 v51, 0x42000000, v51
	v_mul_f32_e32 v52, 0x42000000, v52
	v_mul_f32_e32 v53, 0x42000000, v53
	v_mul_f32_e32 v54, 0x42000000, v54
	v_mul_f32_e32 v55, 0x42000000, v55
	v_mul_f32_e32 v56, 0x42000000, v56
	v_mul_f32_e32 v57, 0x42000000, v57
	v_mul_f32_e32 v58, 0x42000000, v58
	v_mul_f32_e32 v59, 0x42000000, v59
	v_mul_f32_e32 v60, 0x42000000, v60
	v_mul_f32_e32 v61, 0x42000000, v61
	v_mul_f32_e32 v62, 0x42000000, v62
	v_mul_f32_e32 v63, 0x42000000, v63
	v_mul_f32_e32 v64, 0x42000000, v64
	v_mul_f32_e32 v65, 0x42000000, v65
	v_cvt_pk_fp8_f32 v158, v50, v51
	v_cvt_pk_fp8_f32 v159, v54, v55
	v_cvt_pk_fp8_f32 v160, v58, v59
	v_cvt_pk_fp8_f32 v161, v62, v63
	v_cvt_pk_fp8_f32 v158, v52, v53 op_sel:[0,0,1]
	v_cvt_pk_fp8_f32 v159, v56, v57 op_sel:[0,0,1]
	v_cvt_pk_fp8_f32 v160, v60, v61 op_sel:[0,0,1]
	v_cvt_pk_fp8_f32 v161, v64, v65 op_sel:[0,0,1]
	s_waitcnt vmcnt(16)
	v_mul_f32_e32 v66, 0x42000000, v66
	v_mul_f32_e32 v67, 0x42000000, v67
	v_mul_f32_e32 v68, 0x42000000, v68
	v_mul_f32_e32 v69, 0x42000000, v69
	v_mul_f32_e32 v70, 0x42000000, v70
	v_mul_f32_e32 v71, 0x42000000, v71
	v_mul_f32_e32 v72, 0x42000000, v72
	v_mul_f32_e32 v73, 0x42000000, v73
	v_mul_f32_e32 v74, 0x42000000, v74
	v_mul_f32_e32 v75, 0x42000000, v75
	v_mul_f32_e32 v76, 0x42000000, v76
	v_mul_f32_e32 v77, 0x42000000, v77
	v_mul_f32_e32 v78, 0x42000000, v78
	v_mul_f32_e32 v79, 0x42000000, v79
	v_mul_f32_e32 v80, 0x42000000, v80
	v_mul_f32_e32 v81, 0x42000000, v81
	v_cvt_pk_fp8_f32 v162, v66, v67
	v_cvt_pk_fp8_f32 v163, v70, v71
	v_cvt_pk_fp8_f32 v164, v74, v75
	v_cvt_pk_fp8_f32 v165, v78, v79
	v_cvt_pk_fp8_f32 v162, v68, v69 op_sel:[0,0,1]
	v_cvt_pk_fp8_f32 v163, v72, v73 op_sel:[0,0,1]
	v_cvt_pk_fp8_f32 v164, v76, v77 op_sel:[0,0,1]
	v_cvt_pk_fp8_f32 v165, v80, v81 op_sel:[0,0,1]
	s_waitcnt vmcnt(0)
	v_mul_f32_e32 v82, 0x42000000, v82
	v_mul_f32_e32 v83, 0x42000000, v83
	v_mul_f32_e32 v84, 0x42000000, v84
	v_mul_f32_e32 v85, 0x42000000, v85
	v_mul_f32_e32 v86, 0x42000000, v86
	v_mul_f32_e32 v87, 0x42000000, v87
	v_mul_f32_e32 v88, 0x42000000, v88
	v_mul_f32_e32 v89, 0x42000000, v89
	v_mul_f32_e32 v90, 0x42000000, v90
	v_mul_f32_e32 v91, 0x42000000, v91
	v_mul_f32_e32 v92, 0x42000000, v92
	v_mul_f32_e32 v93, 0x42000000, v93
	v_mul_f32_e32 v94, 0x42000000, v94
	v_mul_f32_e32 v95, 0x42000000, v95
	v_mul_f32_e32 v96, 0x42000000, v96
	v_mul_f32_e32 v97, 0x42000000, v97
	v_cvt_pk_fp8_f32 v166, v82, v83
	v_cvt_pk_fp8_f32 v167, v86, v87
	v_cvt_pk_fp8_f32 v168, v90, v91
	v_cvt_pk_fp8_f32 v169, v94, v95
	v_cvt_pk_fp8_f32 v166, v84, v85 op_sel:[0,0,1]
	v_cvt_pk_fp8_f32 v167, v88, v89 op_sel:[0,0,1]
	v_cvt_pk_fp8_f32 v168, v92, v93 op_sel:[0,0,1]
	v_cvt_pk_fp8_f32 v169, v96, v97 op_sel:[0,0,1]
	s_mov_b32 vcc_lo, 0xaaaaaaaa
	s_mov_b32 vcc_hi, 0xaaaaaaaa
	s_nop 1
	v_cndmask_b32_dpp v170, v154, v158, vcc quad_perm:[1,0,3,2] row_mask:0xf bank_mask:0xf
	v_cndmask_b32_dpp v174, v162, v166, vcc quad_perm:[1,0,3,2] row_mask:0xf bank_mask:0xf
	v_cndmask_b32_dpp v171, v155, v159, vcc quad_perm:[1,0,3,2] row_mask:0xf bank_mask:0xf
	v_cndmask_b32_dpp v175, v163, v167, vcc quad_perm:[1,0,3,2] row_mask:0xf bank_mask:0xf
	v_cndmask_b32_dpp v172, v156, v160, vcc quad_perm:[1,0,3,2] row_mask:0xf bank_mask:0xf
	v_cndmask_b32_dpp v176, v164, v168, vcc quad_perm:[1,0,3,2] row_mask:0xf bank_mask:0xf
	v_cndmask_b32_dpp v173, v157, v161, vcc quad_perm:[1,0,3,2] row_mask:0xf bank_mask:0xf
	v_cndmask_b32_dpp v177, v165, v169, vcc quad_perm:[1,0,3,2] row_mask:0xf bank_mask:0xf
	s_mov_b32 vcc_lo, 0x55555555
	s_mov_b32 vcc_hi, 0x55555555
	s_nop 1
	v_cndmask_b32_dpp v154, v158, v154, vcc quad_perm:[1,0,3,2] row_mask:0xf bank_mask:0xf
	v_cndmask_b32_dpp v162, v166, v162, vcc quad_perm:[1,0,3,2] row_mask:0xf bank_mask:0xf
	v_cndmask_b32_dpp v155, v159, v155, vcc quad_perm:[1,0,3,2] row_mask:0xf bank_mask:0xf
	v_cndmask_b32_dpp v163, v167, v163, vcc quad_perm:[1,0,3,2] row_mask:0xf bank_mask:0xf
	v_cndmask_b32_dpp v156, v160, v156, vcc quad_perm:[1,0,3,2] row_mask:0xf bank_mask:0xf
	v_cndmask_b32_dpp v164, v168, v164, vcc quad_perm:[1,0,3,2] row_mask:0xf bank_mask:0xf
	v_cndmask_b32_dpp v157, v161, v157, vcc quad_perm:[1,0,3,2] row_mask:0xf bank_mask:0xf
	v_cndmask_b32_dpp v165, v169, v165, vcc quad_perm:[1,0,3,2] row_mask:0xf bank_mask:0xf
	s_mov_b32 vcc_lo, 0xcccccccc
	s_mov_b32 vcc_hi, 0xcccccccc
	s_nop 1
	v_cndmask_b32_dpp v158, v154, v162, vcc quad_perm:[2,3,0,1] row_mask:0xf bank_mask:0xf
	v_cndmask_b32_dpp v166, v170, v174, vcc quad_perm:[2,3,0,1] row_mask:0xf bank_mask:0xf
	v_cndmask_b32_dpp v159, v155, v163, vcc quad_perm:[2,3,0,1] row_mask:0xf bank_mask:0xf
	v_cndmask_b32_dpp v167, v171, v175, vcc quad_perm:[2,3,0,1] row_mask:0xf bank_mask:0xf
	v_cndmask_b32_dpp v160, v156, v164, vcc quad_perm:[2,3,0,1] row_mask:0xf bank_mask:0xf
	v_cndmask_b32_dpp v168, v172, v176, vcc quad_perm:[2,3,0,1] row_mask:0xf bank_mask:0xf
	v_cndmask_b32_dpp v161, v157, v165, vcc quad_perm:[2,3,0,1] row_mask:0xf bank_mask:0xf
	v_cndmask_b32_dpp v169, v173, v177, vcc quad_perm:[2,3,0,1] row_mask:0xf bank_mask:0xf
	s_mov_b32 vcc_lo, 0x33333333
	s_mov_b32 vcc_hi, 0x33333333
	s_nop 1
	v_cndmask_b32_dpp v154, v162, v154, vcc quad_perm:[2,3,0,1] row_mask:0xf bank_mask:0xf
	v_cndmask_b32_dpp v170, v174, v170, vcc quad_perm:[2,3,0,1] row_mask:0xf bank_mask:0xf
	v_cndmask_b32_dpp v155, v163, v155, vcc quad_perm:[2,3,0,1] row_mask:0xf bank_mask:0xf
	v_cndmask_b32_dpp v171, v175, v171, vcc quad_perm:[2,3,0,1] row_mask:0xf bank_mask:0xf
	v_cndmask_b32_dpp v156, v164, v156, vcc quad_perm:[2,3,0,1] row_mask:0xf bank_mask:0xf
	v_cndmask_b32_dpp v172, v176, v172, vcc quad_perm:[2,3,0,1] row_mask:0xf bank_mask:0xf
	v_cndmask_b32_dpp v157, v165, v157, vcc quad_perm:[2,3,0,1] row_mask:0xf bank_mask:0xf
	v_cndmask_b32_dpp v173, v177, v173, vcc quad_perm:[2,3,0,1] row_mask:0xf bank_mask:0xf
	global_store_dwordx4 v179, v[154:157], s[82:83] sc1
	global_store_dwordx4 v180, v[170:173], s[82:83] sc1
	global_store_dwordx4 v181, v[158:161], s[82:83] sc1
	global_store_dwordx4 v190, v[166:169], s[82:83] sc1
	v_readlane_b32 s2, v239, 0
	s_lshr_b32 s2, s2, 6
	s_add_i32 s2, s2, 6
	s_cmp_gt_u32 s2, 13
	s_cbranch_scc1 .Lhw_seam2_done
	s_add_i32 s2, s2, 28
	s_mul_i32 s2, s2, s74
	v_readlane_b32 s9, v239, 23
	s_lshr_b32 s9, s9, 3
	s_add_i32 s2, s2, s9
	s_cmp_gt_u32 s2, 24575
	s_cbranch_scc1 .Lhw_seam2_done
	v_mbcnt_lo_u32_b32 v178, -1, 0
	v_mbcnt_hi_u32_b32 v178, -1, v178
	v_and_b32_e32 v179, 60, v178
	v_lshlrev_b32_e32 v179, 10, v179
	v_and_b32_e32 v180, 3, v178
	v_lshl_or_b32 v179, v180, 4, v179
	v_add_u32_e32 v180, 0x400, v179
	v_add_u32_e32 v181, 0x800, v179
	v_add_u32_e32 v190, 0xc00, v179
	v_lshlrev_b32_e32 v178, 2, v178
	s_cmp_lt_u32 s2, 16384
	s_cbranch_scc0 .Lhw_dn_s2_1
	s_lshr_b32 s9, s2, 9
	s_bfe_u32 s32, s2, 0x40005
	s_and_b32 s53, s2, 31
	s_lshl_b32 s69, s9, 23
	s_lshl_b32 s100, s32, 19
	s_add_i32 s69, s69, s100
	s_lshl_b32 s100, s53, 8
	s_add_i32 s69, s69, s100
	s_lshl_b32 s98, s9, 11
	s_bfe_u32 s100, s53, 0x30001
	s_lshl_b32 s100, s100, 8
	s_add_i32 s98, s98, s100
	s_lshr_b32 s100, s53, 4
	s_lshl_b32 s100, s100, 7
	s_add_i32 s98, s98, s100
	s_and_b32 s100, s53, 1
	s_lshl_b32 s100, s100, 6
	s_add_i32 s98, s98, s100
	s_lshl_b32 s98, s98, 10
	s_lshl_b32 s100, s32, 6
	s_add_i32 s98, s98, s100
	s_add_i32 s98, s98, 0x2000000
	v_readlane_b32 s82, v239, 11
	v_readlane_b32 s83, v239, 12
	s_movk_i32 s89, 8192
	s_branch .Lhw_go_s2_1

.Lhw_go_s3_0:
	s_add_u32 s100, s82, s69
	s_addc_u32 s101, s83, 0
	v_readlane_b32 s82, v239, 44
	v_readlane_b32 s83, v239, 45
	s_add_u32 s82, s82, s98
	s_addc_u32 s83, s83, 0
	global_load_dword v34, v178, s[100:101] nt
	s_add_u32 s100, s100, s89
	s_addc_u32 s101, s101, 0
	global_load_dword v35, v178, s[100:101] nt
	s_add_u32 s100, s100, s89
	s_addc_u32 s101, s101, 0
	global_load_dword v36, v178, s[100:101] nt
	s_add_u32 s100, s100, s89
	s_addc_u32 s101, s101, 0
	global_load_dword v37, v178, s[100:101] nt
	s_add_u32 s100, s100, s89
	s_addc_u32 s101, s101, 0
	global_load_dword v38, v178, s[100:101] nt
	s_add_u32 s100, s100, s89
	s_addc_u32 s101, s101, 0
	global_load_dword v39, v178, s[100:101] nt
	s_add_u32 s100, s100, s89
	s_addc_u32 s101, s101, 0
	global_load_dword v40, v178, s[100:101] nt
	s_add_u32 s100, s100, s89
	s_addc_u32 s101, s101, 0
	global_load_dword v41, v178, s[100:101] nt
	s_add_u32 s100, s100, s89
	s_addc_u32 s101, s101, 0
	global_load_dword v42, v178, s[100:101] nt
	s_add_u32 s100, s100, s89
	s_addc_u32 s101, s101, 0
	global_load_dword v43, v178, s[100:101] nt
	s_add_u32 s100, s100, s89
	s_addc_u32 s101, s101, 0
	global_load_dword v44, v178, s[100:101] nt
	s_add_u32 s100, s100, s89
	s_addc_u32 s101, s101, 0
	global_load_dword v45, v178, s[100:101] nt
	s_add_u32 s100, s100, s89
	s_addc_u32 s101, s101, 0
	global_load_dword v46, v178, s[100:101] nt
	s_add_u32 s100, s100, s89
	s_addc_u32 s101, s101, 0
	global_load_dword v47, v178, s[100:101] nt
	s_add_u32 s100, s100, s89
	s_addc_u32 s101, s101, 0
	global_load_dword v48, v178, s[100:101] nt
	s_add_u32 s100, s100, s89
	s_addc_u32 s101, s101, 0
	global_load_dword v49, v178, s[100:101] nt
	s_add_u32 s100, s100, s89
	s_addc_u32 s101, s101, 0
	global_load_dword v50, v178, s[100:101] nt
	s_add_u32 s100, s100, s89
	s_addc_u32 s101, s101, 0
	global_load_dword v51, v178, s[100:101] nt
	s_add_u32 s100, s100, s89
	s_addc_u32 s101, s101, 0
	global_load_dword v52, v178, s[100:101] nt
	s_add_u32 s100, s100, s89
	s_addc_u32 s101, s101, 0
	global_load_dword v53, v178, s[100:101] nt
	s_add_u32 s100, s100, s89
	s_addc_u32 s101, s101, 0
	global_load_dword v54, v178, s[100:101] nt
	s_add_u32 s100, s100, s89
	s_addc_u32 s101, s101, 0
	global_load_dword v55, v178, s[100:101] nt
	s_add_u32 s100, s100, s89
	s_addc_u32 s101, s101, 0
	global_load_dword v56, v178, s[100:101] nt
	s_add_u32 s100, s100, s89
	s_addc_u32 s101, s101, 0
	global_load_dword v57, v178, s[100:101] nt
	s_add_u32 s100, s100, s89
	s_addc_u32 s101, s101, 0
	global_load_dword v58, v178, s[100:101] nt
	s_add_u32 s100, s100, s89
	s_addc_u32 s101, s101, 0
	global_load_dword v59, v178, s[100:101] nt
	s_add_u32 s100, s100, s89
	s_addc_u32 s101, s101, 0
	global_load_dword v60, v178, s[100:101] nt
	s_add_u32 s100, s100, s89
	s_addc_u32 s101, s101, 0
	global_load_dword v61, v178, s[100:101] nt
	s_add_u32 s100, s100, s89
	s_addc_u32 s101, s101, 0
	global_load_dword v62, v178, s[100:101] nt
	s_add_u32 s100, s100, s89
	s_addc_u32 s101, s101, 0
	global_load_dword v63, v178, s[100:101] nt
	s_add_u32 s100, s100, s89
	s_addc_u32 s101, s101, 0
	global_load_dword v64, v178, s[100:101] nt
	s_add_u32 s100, s100, s89
	s_addc_u32 s101, s101, 0
	global_load_dword v65, v178, s[100:101] nt
	s_add_u32 s100, s100, s89
	s_addc_u32 s101, s101, 0
	global_load_dword v66, v178, s[100:101] nt
	s_add_u32 s100, s100, s89
	s_addc_u32 s101, s101, 0
	global_load_dword v67, v178, s[100:101] nt
	s_add_u32 s100, s100, s89
	s_addc_u32 s101, s101, 0
	global_load_dword v68, v178, s[100:101] nt
	s_add_u32 s100, s100, s89
	s_addc_u32 s101, s101, 0
	global_load_dword v69, v178, s[100:101] nt
	s_add_u32 s100, s100, s89
	s_addc_u32 s101, s101, 0
	global_load_dword v70, v178, s[100:101] nt
	s_add_u32 s100, s100, s89
	s_addc_u32 s101, s101, 0
	global_load_dword v71, v178, s[100:101] nt
	s_add_u32 s100, s100, s89
	s_addc_u32 s101, s101, 0
	global_load_dword v72, v178, s[100:101] nt
	s_add_u32 s100, s100, s89
	s_addc_u32 s101, s101, 0
	global_load_dword v73, v178, s[100:101] nt
	s_add_u32 s100, s100, s89
	s_addc_u32 s101, s101, 0
	global_load_dword v74, v178, s[100:101] nt
	s_add_u32 s100, s100, s89
	s_addc_u32 s101, s101, 0
	global_load_dword v75, v178, s[100:101] nt
	s_add_u32 s100, s100, s89
	s_addc_u32 s101, s101, 0
	global_load_dword v76, v178, s[100:101] nt
	s_add_u32 s100, s100, s89
	s_addc_u32 s101, s101, 0
	global_load_dword v77, v178, s[100:101] nt
	s_add_u32 s100, s100, s89
	s_addc_u32 s101, s101, 0
	global_load_dword v78, v178, s[100:101] nt
	s_add_u32 s100, s100, s89
	s_addc_u32 s101, s101, 0
	global_load_dword v79, v178, s[100:101] nt
	s_add_u32 s100, s100, s89
	s_addc_u32 s101, s101, 0
	global_load_dword v80, v178, s[100:101] nt
	s_add_u32 s100, s100, s89
	s_addc_u32 s101, s101, 0
	global_load_dword v81, v178, s[100:101] nt
	s_add_u32 s100, s100, s89
	s_addc_u32 s101, s101, 0
	global_load_dword v82, v178, s[100:101] nt
	s_add_u32 s100, s100, s89
	s_addc_u32 s101, s101, 0
	global_load_dword v83, v178, s[100:101] nt
	s_add_u32 s100, s100, s89
	s_addc_u32 s101, s101, 0
	global_load_dword v84, v178, s[100:101] nt
	s_add_u32 s100, s100, s89
	s_addc_u32 s101, s101, 0
	global_load_dword v85, v178, s[100:101] nt
	s_add_u32 s100, s100, s89
	s_addc_u32 s101, s101, 0
	global_load_dword v86, v178, s[100:101] nt
	s_add_u32 s100, s100, s89
	s_addc_u32 s101, s101, 0
	global_load_dword v87, v178, s[100:101] nt
	s_add_u32 s100, s100, s89
	s_addc_u32 s101, s101, 0
	global_load_dword v88, v178, s[100:101] nt
	s_add_u32 s100, s100, s89
	s_addc_u32 s101, s101, 0
	global_load_dword v89, v178, s[100:101] nt
	s_add_u32 s100, s100, s89
	s_addc_u32 s101, s101, 0
	global_load_dword v90, v178, s[100:101] nt
	s_add_u32 s100, s100, s89
	s_addc_u32 s101, s101, 0
	global_load_dword v91, v178, s[100:101] nt
	s_add_u32 s100, s100, s89
	s_addc_u32 s101, s101, 0
	global_load_dword v92, v178, s[100:101] nt
	s_add_u32 s100, s100, s89
	s_addc_u32 s101, s101, 0
	global_load_dword v93, v178, s[100:101] nt
	s_add_u32 s100, s100, s89
	s_addc_u32 s101, s101, 0
	global_load_dword v94, v178, s[100:101] nt
	s_add_u32 s100, s100, s89
	s_addc_u32 s101, s101, 0
	global_load_dword v95, v178, s[100:101] nt
	s_add_u32 s100, s100, s89
	s_addc_u32 s101, s101, 0
	global_load_dword v96, v178, s[100:101] nt
	s_add_u32 s100, s100, s89
	s_addc_u32 s101, s101, 0
	global_load_dword v97, v178, s[100:101] nt
	s_add_u32 s100, s100, s89
	s_addc_u32 s101, s101, 0
	s_waitcnt vmcnt(48)
	v_mul_f32_e32 v34, 0x42000000, v34
	v_mul_f32_e32 v35, 0x42000000, v35
	v_mul_f32_e32 v36, 0x42000000, v36
	v_mul_f32_e32 v37, 0x42000000, v37
	v_mul_f32_e32 v38, 0x42000000, v38
	v_mul_f32_e32 v39, 0x42000000, v39
	v_mul_f32_e32 v40, 0x42000000, v40
	v_mul_f32_e32 v41, 0x42000000, v41
	v_mul_f32_e32 v42, 0x42000000, v42
	v_mul_f32_e32 v43, 0x42000000, v43
	v_mul_f32_e32 v44, 0x42000000, v44
	v_mul_f32_e32 v45, 0x42000000, v45
	v_mul_f32_e32 v46, 0x42000000, v46
	v_mul_f32_e32 v47, 0x42000000, v47
	v_mul_f32_e32 v48, 0x42000000, v48
	v_mul_f32_e32 v49, 0x42000000, v49
	v_cvt_pk_fp8_f32 v154, v34, v35
	v_cvt_pk_fp8_f32 v155, v38, v39
	v_cvt_pk_fp8_f32 v156, v42, v43
	v_cvt_pk_fp8_f32 v157, v46, v47
	v_cvt_pk_fp8_f32 v154, v36, v37 op_sel:[0,0,1]
	v_cvt_pk_fp8_f32 v155, v40, v41 op_sel:[0,0,1]
	v_cvt_pk_fp8_f32 v156, v44, v45 op_sel:[0,0,1]
	v_cvt_pk_fp8_f32 v157, v48, v49 op_sel:[0,0,1]
	s_waitcnt vmcnt(32)
	v_mul_f32_e32 v50, 0x42000000, v50
	v_mul_f32_e32 v51, 0x42000000, v51
	v_mul_f32_e32 v52, 0x42000000, v52
	v_mul_f32_e32 v53, 0x42000000, v53
	v_mul_f32_e32 v54, 0x42000000, v54
	v_mul_f32_e32 v55, 0x42000000, v55
	v_mul_f32_e32 v56, 0x42000000, v56
	v_mul_f32_e32 v57, 0x42000000, v57
	v_mul_f32_e32 v58, 0x42000000, v58
	v_mul_f32_e32 v59, 0x42000000, v59
	v_mul_f32_e32 v60, 0x42000000, v60
	v_mul_f32_e32 v61, 0x42000000, v61
	v_mul_f32_e32 v62, 0x42000000, v62
	v_mul_f32_e32 v63, 0x42000000, v63
	v_mul_f32_e32 v64, 0x42000000, v64
	v_mul_f32_e32 v65, 0x42000000, v65
	v_cvt_pk_fp8_f32 v158, v50, v51
	v_cvt_pk_fp8_f32 v159, v54, v55
	v_cvt_pk_fp8_f32 v160, v58, v59
	v_cvt_pk_fp8_f32 v161, v62, v63
	v_cvt_pk_fp8_f32 v158, v52, v53 op_sel:[0,0,1]
	v_cvt_pk_fp8_f32 v159, v56, v57 op_sel:[0,0,1]
	v_cvt_pk_fp8_f32 v160, v60, v61 op_sel:[0,0,1]
	v_cvt_pk_fp8_f32 v161, v64, v65 op_sel:[0,0,1]
	s_waitcnt vmcnt(16)
	v_mul_f32_e32 v66, 0x42000000, v66
	v_mul_f32_e32 v67, 0x42000000, v67
	v_mul_f32_e32 v68, 0x42000000, v68
	v_mul_f32_e32 v69, 0x42000000, v69
	v_mul_f32_e32 v70, 0x42000000, v70
	v_mul_f32_e32 v71, 0x42000000, v71
	v_mul_f32_e32 v72, 0x42000000, v72
	v_mul_f32_e32 v73, 0x42000000, v73
	v_mul_f32_e32 v74, 0x42000000, v74
	v_mul_f32_e32 v75, 0x42000000, v75
	v_mul_f32_e32 v76, 0x42000000, v76
	v_mul_f32_e32 v77, 0x42000000, v77
	v_mul_f32_e32 v78, 0x42000000, v78
	v_mul_f32_e32 v79, 0x42000000, v79
	v_mul_f32_e32 v80, 0x42000000, v80
	v_mul_f32_e32 v81, 0x42000000, v81
	v_cvt_pk_fp8_f32 v162, v66, v67
	v_cvt_pk_fp8_f32 v163, v70, v71
	v_cvt_pk_fp8_f32 v164, v74, v75
	v_cvt_pk_fp8_f32 v165, v78, v79
	v_cvt_pk_fp8_f32 v162, v68, v69 op_sel:[0,0,1]
	v_cvt_pk_fp8_f32 v163, v72, v73 op_sel:[0,0,1]
	v_cvt_pk_fp8_f32 v164, v76, v77 op_sel:[0,0,1]
	v_cvt_pk_fp8_f32 v165, v80, v81 op_sel:[0,0,1]
	s_waitcnt vmcnt(0)
	v_mul_f32_e32 v82, 0x42000000, v82
	v_mul_f32_e32 v83, 0x42000000, v83
	v_mul_f32_e32 v84, 0x42000000, v84
	v_mul_f32_e32 v85, 0x42000000, v85
	v_mul_f32_e32 v86, 0x42000000, v86
	v_mul_f32_e32 v87, 0x42000000, v87
	v_mul_f32_e32 v88, 0x42000000, v88
	v_mul_f32_e32 v89, 0x42000000, v89
	v_mul_f32_e32 v90, 0x42000000, v90
	v_mul_f32_e32 v91, 0x42000000, v91
	v_mul_f32_e32 v92, 0x42000000, v92
	v_mul_f32_e32 v93, 0x42000000, v93
	v_mul_f32_e32 v94, 0x42000000, v94
	v_mul_f32_e32 v95, 0x42000000, v95
	v_mul_f32_e32 v96, 0x42000000, v96
	v_mul_f32_e32 v97, 0x42000000, v97
	v_cvt_pk_fp8_f32 v166, v82, v83
	v_cvt_pk_fp8_f32 v167, v86, v87
	v_cvt_pk_fp8_f32 v168, v90, v91
	v_cvt_pk_fp8_f32 v169, v94, v95
	v_cvt_pk_fp8_f32 v166, v84, v85 op_sel:[0,0,1]
	v_cvt_pk_fp8_f32 v167, v88, v89 op_sel:[0,0,1]
	v_cvt_pk_fp8_f32 v168, v92, v93 op_sel:[0,0,1]
	v_cvt_pk_fp8_f32 v169, v96, v97 op_sel:[0,0,1]
	s_mov_b32 vcc_lo, 0xaaaaaaaa
	s_mov_b32 vcc_hi, 0xaaaaaaaa
	s_nop 1
	v_cndmask_b32_dpp v170, v154, v158, vcc quad_perm:[1,0,3,2] row_mask:0xf bank_mask:0xf
	v_cndmask_b32_dpp v174, v162, v166, vcc quad_perm:[1,0,3,2] row_mask:0xf bank_mask:0xf
	v_cndmask_b32_dpp v171, v155, v159, vcc quad_perm:[1,0,3,2] row_mask:0xf bank_mask:0xf
	v_cndmask_b32_dpp v175, v163, v167, vcc quad_perm:[1,0,3,2] row_mask:0xf bank_mask:0xf
	v_cndmask_b32_dpp v172, v156, v160, vcc quad_perm:[1,0,3,2] row_mask:0xf bank_mask:0xf
	v_cndmask_b32_dpp v176, v164, v168, vcc quad_perm:[1,0,3,2] row_mask:0xf bank_mask:0xf
	v_cndmask_b32_dpp v173, v157, v161, vcc quad_perm:[1,0,3,2] row_mask:0xf bank_mask:0xf
	v_cndmask_b32_dpp v177, v165, v169, vcc quad_perm:[1,0,3,2] row_mask:0xf bank_mask:0xf
	s_mov_b32 vcc_lo, 0x55555555
	s_mov_b32 vcc_hi, 0x55555555
	s_nop 1
	v_cndmask_b32_dpp v154, v158, v154, vcc quad_perm:[1,0,3,2] row_mask:0xf bank_mask:0xf
	v_cndmask_b32_dpp v162, v166, v162, vcc quad_perm:[1,0,3,2] row_mask:0xf bank_mask:0xf
	v_cndmask_b32_dpp v155, v159, v155, vcc quad_perm:[1,0,3,2] row_mask:0xf bank_mask:0xf
	v_cndmask_b32_dpp v163, v167, v163, vcc quad_perm:[1,0,3,2] row_mask:0xf bank_mask:0xf
	v_cndmask_b32_dpp v156, v160, v156, vcc quad_perm:[1,0,3,2] row_mask:0xf bank_mask:0xf
	v_cndmask_b32_dpp v164, v168, v164, vcc quad_perm:[1,0,3,2] row_mask:0xf bank_mask:0xf
	v_cndmask_b32_dpp v157, v161, v157, vcc quad_perm:[1,0,3,2] row_mask:0xf bank_mask:0xf
	v_cndmask_b32_dpp v165, v169, v165, vcc quad_perm:[1,0,3,2] row_mask:0xf bank_mask:0xf
	s_mov_b32 vcc_lo, 0xcccccccc
	s_mov_b32 vcc_hi, 0xcccccccc
	s_nop 1
	v_cndmask_b32_dpp v158, v154, v162, vcc quad_perm:[2,3,0,1] row_mask:0xf bank_mask:0xf
	v_cndmask_b32_dpp v166, v170, v174, vcc quad_perm:[2,3,0,1] row_mask:0xf bank_mask:0xf
	v_cndmask_b32_dpp v159, v155, v163, vcc quad_perm:[2,3,0,1] row_mask:0xf bank_mask:0xf
	v_cndmask_b32_dpp v167, v171, v175, vcc quad_perm:[2,3,0,1] row_mask:0xf bank_mask:0xf
	v_cndmask_b32_dpp v160, v156, v164, vcc quad_perm:[2,3,0,1] row_mask:0xf bank_mask:0xf
	v_cndmask_b32_dpp v168, v172, v176, vcc quad_perm:[2,3,0,1] row_mask:0xf bank_mask:0xf
	v_cndmask_b32_dpp v161, v157, v165, vcc quad_perm:[2,3,0,1] row_mask:0xf bank_mask:0xf
	v_cndmask_b32_dpp v169, v173, v177, vcc quad_perm:[2,3,0,1] row_mask:0xf bank_mask:0xf
	s_mov_b32 vcc_lo, 0x33333333
	s_mov_b32 vcc_hi, 0x33333333
	s_nop 1
	v_cndmask_b32_dpp v154, v162, v154, vcc quad_perm:[2,3,0,1] row_mask:0xf bank_mask:0xf
	v_cndmask_b32_dpp v170, v174, v170, vcc quad_perm:[2,3,0,1] row_mask:0xf bank_mask:0xf
	v_cndmask_b32_dpp v155, v163, v155, vcc quad_perm:[2,3,0,1] row_mask:0xf bank_mask:0xf
	v_cndmask_b32_dpp v171, v175, v171, vcc quad_perm:[2,3,0,1] row_mask:0xf bank_mask:0xf
	v_cndmask_b32_dpp v156, v164, v156, vcc quad_perm:[2,3,0,1] row_mask:0xf bank_mask:0xf
	v_cndmask_b32_dpp v172, v176, v172, vcc quad_perm:[2,3,0,1] row_mask:0xf bank_mask:0xf
	v_cndmask_b32_dpp v157, v165, v157, vcc quad_perm:[2,3,0,1] row_mask:0xf bank_mask:0xf
	v_cndmask_b32_dpp v173, v177, v173, vcc quad_perm:[2,3,0,1] row_mask:0xf bank_mask:0xf
	global_store_dwordx4 v179, v[154:157], s[82:83] sc1
	global_store_dwordx4 v180, v[170:173], s[82:83] sc1
	global_store_dwordx4 v181, v[158:161], s[82:83] sc1
	global_store_dwordx4 v190, v[166:169], s[82:83] sc1
	v_readlane_b32 s2, v239, 0
	s_lshr_b32 s2, s2, 6
	s_add_i32 s2, s2, 6
	s_cmp_gt_u32 s2, 13
	s_cbranch_scc1 .Lhw_seam3_done
	s_add_i32 s2, s2, 42
	s_mul_i32 s2, s2, s74
	v_readlane_b32 s9, v239, 23
	s_lshr_b32 s9, s9, 3
	s_add_i32 s2, s2, s9
	s_cmp_gt_u32 s2, 24575
	s_cbranch_scc1 .Lhw_seam3_done
	v_mbcnt_lo_u32_b32 v178, -1, 0
	v_mbcnt_hi_u32_b32 v178, -1, v178
	v_and_b32_e32 v179, 60, v178
	v_lshlrev_b32_e32 v179, 10, v179
	v_and_b32_e32 v180, 3, v178
	v_lshl_or_b32 v179, v180, 4, v179
	v_add_u32_e32 v180, 0x400, v179
	v_add_u32_e32 v181, 0x800, v179
	v_add_u32_e32 v190, 0xc00, v179
	v_lshlrev_b32_e32 v178, 2, v178
	s_cmp_lt_u32 s2, 16384
	s_cbranch_scc0 .Lhw_dn_s3_1
	s_lshr_b32 s9, s2, 9
	s_bfe_u32 s32, s2, 0x40005
	s_and_b32 s53, s2, 31
	s_lshl_b32 s69, s9, 23
	s_lshl_b32 s100, s32, 19
	s_add_i32 s69, s69, s100
	s_lshl_b32 s100, s53, 8
	s_add_i32 s69, s69, s100
	s_lshl_b32 s98, s9, 11
	s_bfe_u32 s100, s53, 0x30001
	s_lshl_b32 s100, s100, 8
	s_add_i32 s98, s98, s100
	s_lshr_b32 s100, s53, 4
	s_lshl_b32 s100, s100, 7
	s_add_i32 s98, s98, s100
	s_and_b32 s100, s53, 1
	s_lshl_b32 s100, s100, 6
	s_add_i32 s98, s98, s100
	s_lshl_b32 s98, s98, 10
	s_lshl_b32 s100, s32, 6
	s_add_i32 s98, s98, s100
	s_add_i32 s98, s98, 0x2000000
	v_readlane_b32 s82, v239, 11
	v_readlane_b32 s83, v239, 12
	s_movk_i32 s89, 8192
	s_branch .Lhw_go_s3_1

.Lhw_go_s4_0:
	s_add_u32 s100, s82, s69
	s_addc_u32 s101, s83, 0
	v_readlane_b32 s82, v239, 44
	v_readlane_b32 s83, v239, 45
	s_add_u32 s82, s82, s98
	s_addc_u32 s83, s83, 0
	global_load_dword v34, v178, s[100:101] nt
	s_add_u32 s100, s100, s89
	s_addc_u32 s101, s101, 0
	global_load_dword v35, v178, s[100:101] nt
	s_add_u32 s100, s100, s89
	s_addc_u32 s101, s101, 0
	global_load_dword v36, v178, s[100:101] nt
	s_add_u32 s100, s100, s89
	s_addc_u32 s101, s101, 0
	global_load_dword v37, v178, s[100:101] nt
	s_add_u32 s100, s100, s89
	s_addc_u32 s101, s101, 0
	global_load_dword v38, v178, s[100:101] nt
	s_add_u32 s100, s100, s89
	s_addc_u32 s101, s101, 0
	global_load_dword v39, v178, s[100:101] nt
	s_add_u32 s100, s100, s89
	s_addc_u32 s101, s101, 0
	global_load_dword v40, v178, s[100:101] nt
	s_add_u32 s100, s100, s89
	s_addc_u32 s101, s101, 0
	global_load_dword v41, v178, s[100:101] nt
	s_add_u32 s100, s100, s89
	s_addc_u32 s101, s101, 0
	global_load_dword v42, v178, s[100:101] nt
	s_add_u32 s100, s100, s89
	s_addc_u32 s101, s101, 0
	global_load_dword v43, v178, s[100:101] nt
	s_add_u32 s100, s100, s89
	s_addc_u32 s101, s101, 0
	global_load_dword v44, v178, s[100:101] nt
	s_add_u32 s100, s100, s89
	s_addc_u32 s101, s101, 0
	global_load_dword v45, v178, s[100:101] nt
	s_add_u32 s100, s100, s89
	s_addc_u32 s101, s101, 0
	global_load_dword v46, v178, s[100:101] nt
	s_add_u32 s100, s100, s89
	s_addc_u32 s101, s101, 0
	global_load_dword v47, v178, s[100:101] nt
	s_add_u32 s100, s100, s89
	s_addc_u32 s101, s101, 0
	global_load_dword v48, v178, s[100:101] nt
	s_add_u32 s100, s100, s89
	s_addc_u32 s101, s101, 0
	global_load_dword v49, v178, s[100:101] nt
	s_add_u32 s100, s100, s89
	s_addc_u32 s101, s101, 0
	global_load_dword v50, v178, s[100:101] nt
	s_add_u32 s100, s100, s89
	s_addc_u32 s101, s101, 0
	global_load_dword v51, v178, s[100:101] nt
	s_add_u32 s100, s100, s89
	s_addc_u32 s101, s101, 0
	global_load_dword v52, v178, s[100:101] nt
	s_add_u32 s100, s100, s89
	s_addc_u32 s101, s101, 0
	global_load_dword v53, v178, s[100:101] nt
	s_add_u32 s100, s100, s89
	s_addc_u32 s101, s101, 0
	global_load_dword v54, v178, s[100:101] nt
	s_add_u32 s100, s100, s89
	s_addc_u32 s101, s101, 0
	global_load_dword v55, v178, s[100:101] nt
	s_add_u32 s100, s100, s89
	s_addc_u32 s101, s101, 0
	global_load_dword v56, v178, s[100:101] nt
	s_add_u32 s100, s100, s89
	s_addc_u32 s101, s101, 0
	global_load_dword v57, v178, s[100:101] nt
	s_add_u32 s100, s100, s89
	s_addc_u32 s101, s101, 0
	global_load_dword v58, v178, s[100:101] nt
	s_add_u32 s100, s100, s89
	s_addc_u32 s101, s101, 0
	global_load_dword v59, v178, s[100:101] nt
	s_add_u32 s100, s100, s89
	s_addc_u32 s101, s101, 0
	global_load_dword v60, v178, s[100:101] nt
	s_add_u32 s100, s100, s89
	s_addc_u32 s101, s101, 0
	global_load_dword v61, v178, s[100:101] nt
	s_add_u32 s100, s100, s89
	s_addc_u32 s101, s101, 0
	global_load_dword v62, v178, s[100:101] nt
	s_add_u32 s100, s100, s89
	s_addc_u32 s101, s101, 0
	global_load_dword v63, v178, s[100:101] nt
	s_add_u32 s100, s100, s89
	s_addc_u32 s101, s101, 0
	global_load_dword v64, v178, s[100:101] nt
	s_add_u32 s100, s100, s89
	s_addc_u32 s101, s101, 0
	global_load_dword v65, v178, s[100:101] nt
	s_add_u32 s100, s100, s89
	s_addc_u32 s101, s101, 0
	global_load_dword v66, v178, s[100:101] nt
	s_add_u32 s100, s100, s89
	s_addc_u32 s101, s101, 0
	global_load_dword v67, v178, s[100:101] nt
	s_add_u32 s100, s100, s89
	s_addc_u32 s101, s101, 0
	global_load_dword v68, v178, s[100:101] nt
	s_add_u32 s100, s100, s89
	s_addc_u32 s101, s101, 0
	global_load_dword v69, v178, s[100:101] nt
	s_add_u32 s100, s100, s89
	s_addc_u32 s101, s101, 0
	global_load_dword v70, v178, s[100:101] nt
	s_add_u32 s100, s100, s89
	s_addc_u32 s101, s101, 0
	global_load_dword v71, v178, s[100:101] nt
	s_add_u32 s100, s100, s89
	s_addc_u32 s101, s101, 0
	global_load_dword v72, v178, s[100:101] nt
	s_add_u32 s100, s100, s89
	s_addc_u32 s101, s101, 0
	global_load_dword v73, v178, s[100:101] nt
	s_add_u32 s100, s100, s89
	s_addc_u32 s101, s101, 0
	global_load_dword v74, v178, s[100:101] nt
	s_add_u32 s100, s100, s89
	s_addc_u32 s101, s101, 0
	global_load_dword v75, v178, s[100:101] nt
	s_add_u32 s100, s100, s89
	s_addc_u32 s101, s101, 0
	global_load_dword v76, v178, s[100:101] nt
	s_add_u32 s100, s100, s89
	s_addc_u32 s101, s101, 0
	global_load_dword v77, v178, s[100:101] nt
	s_add_u32 s100, s100, s89
	s_addc_u32 s101, s101, 0
	global_load_dword v78, v178, s[100:101] nt
	s_add_u32 s100, s100, s89
	s_addc_u32 s101, s101, 0
	global_load_dword v79, v178, s[100:101] nt
	s_add_u32 s100, s100, s89
	s_addc_u32 s101, s101, 0
	global_load_dword v80, v178, s[100:101] nt
	s_add_u32 s100, s100, s89
	s_addc_u32 s101, s101, 0
	global_load_dword v81, v178, s[100:101] nt
	s_add_u32 s100, s100, s89
	s_addc_u32 s101, s101, 0
	global_load_dword v82, v178, s[100:101] nt
	s_add_u32 s100, s100, s89
	s_addc_u32 s101, s101, 0
	global_load_dword v83, v178, s[100:101] nt
	s_add_u32 s100, s100, s89
	s_addc_u32 s101, s101, 0
	global_load_dword v84, v178, s[100:101] nt
	s_add_u32 s100, s100, s89
	s_addc_u32 s101, s101, 0
	global_load_dword v85, v178, s[100:101] nt
	s_add_u32 s100, s100, s89
	s_addc_u32 s101, s101, 0
	global_load_dword v86, v178, s[100:101] nt
	s_add_u32 s100, s100, s89
	s_addc_u32 s101, s101, 0
	global_load_dword v87, v178, s[100:101] nt
	s_add_u32 s100, s100, s89
	s_addc_u32 s101, s101, 0
	global_load_dword v88, v178, s[100:101] nt
	s_add_u32 s100, s100, s89
	s_addc_u32 s101, s101, 0
	global_load_dword v89, v178, s[100:101] nt
	s_add_u32 s100, s100, s89
	s_addc_u32 s101, s101, 0
	global_load_dword v90, v178, s[100:101] nt
	s_add_u32 s100, s100, s89
	s_addc_u32 s101, s101, 0
	global_load_dword v91, v178, s[100:101] nt
	s_add_u32 s100, s100, s89
	s_addc_u32 s101, s101, 0
	global_load_dword v92, v178, s[100:101] nt
	s_add_u32 s100, s100, s89
	s_addc_u32 s101, s101, 0
	global_load_dword v93, v178, s[100:101] nt
	s_add_u32 s100, s100, s89
	s_addc_u32 s101, s101, 0
	global_load_dword v94, v178, s[100:101] nt
	s_add_u32 s100, s100, s89
	s_addc_u32 s101, s101, 0
	global_load_dword v95, v178, s[100:101] nt
	s_add_u32 s100, s100, s89
	s_addc_u32 s101, s101, 0
	global_load_dword v96, v178, s[100:101] nt
	s_add_u32 s100, s100, s89
	s_addc_u32 s101, s101, 0
	global_load_dword v97, v178, s[100:101] nt
	s_add_u32 s100, s100, s89
	s_addc_u32 s101, s101, 0
	s_waitcnt vmcnt(48)
	v_mul_f32_e32 v34, 0x42000000, v34
	v_mul_f32_e32 v35, 0x42000000, v35
	v_mul_f32_e32 v36, 0x42000000, v36
	v_mul_f32_e32 v37, 0x42000000, v37
	v_mul_f32_e32 v38, 0x42000000, v38
	v_mul_f32_e32 v39, 0x42000000, v39
	v_mul_f32_e32 v40, 0x42000000, v40
	v_mul_f32_e32 v41, 0x42000000, v41
	v_mul_f32_e32 v42, 0x42000000, v42
	v_mul_f32_e32 v43, 0x42000000, v43
	v_mul_f32_e32 v44, 0x42000000, v44
	v_mul_f32_e32 v45, 0x42000000, v45
	v_mul_f32_e32 v46, 0x42000000, v46
	v_mul_f32_e32 v47, 0x42000000, v47
	v_mul_f32_e32 v48, 0x42000000, v48
	v_mul_f32_e32 v49, 0x42000000, v49
	v_cvt_pk_fp8_f32 v154, v34, v35
	v_cvt_pk_fp8_f32 v155, v38, v39
	v_cvt_pk_fp8_f32 v156, v42, v43
	v_cvt_pk_fp8_f32 v157, v46, v47
	v_cvt_pk_fp8_f32 v154, v36, v37 op_sel:[0,0,1]
	v_cvt_pk_fp8_f32 v155, v40, v41 op_sel:[0,0,1]
	v_cvt_pk_fp8_f32 v156, v44, v45 op_sel:[0,0,1]
	v_cvt_pk_fp8_f32 v157, v48, v49 op_sel:[0,0,1]
	s_waitcnt vmcnt(32)
	v_mul_f32_e32 v50, 0x42000000, v50
	v_mul_f32_e32 v51, 0x42000000, v51
	v_mul_f32_e32 v52, 0x42000000, v52
	v_mul_f32_e32 v53, 0x42000000, v53
	v_mul_f32_e32 v54, 0x42000000, v54
	v_mul_f32_e32 v55, 0x42000000, v55
	v_mul_f32_e32 v56, 0x42000000, v56
	v_mul_f32_e32 v57, 0x42000000, v57
	v_mul_f32_e32 v58, 0x42000000, v58
	v_mul_f32_e32 v59, 0x42000000, v59
	v_mul_f32_e32 v60, 0x42000000, v60
	v_mul_f32_e32 v61, 0x42000000, v61
	v_mul_f32_e32 v62, 0x42000000, v62
	v_mul_f32_e32 v63, 0x42000000, v63
	v_mul_f32_e32 v64, 0x42000000, v64
	v_mul_f32_e32 v65, 0x42000000, v65
	v_cvt_pk_fp8_f32 v158, v50, v51
	v_cvt_pk_fp8_f32 v159, v54, v55
	v_cvt_pk_fp8_f32 v160, v58, v59
	v_cvt_pk_fp8_f32 v161, v62, v63
	v_cvt_pk_fp8_f32 v158, v52, v53 op_sel:[0,0,1]
	v_cvt_pk_fp8_f32 v159, v56, v57 op_sel:[0,0,1]
	v_cvt_pk_fp8_f32 v160, v60, v61 op_sel:[0,0,1]
	v_cvt_pk_fp8_f32 v161, v64, v65 op_sel:[0,0,1]
	s_waitcnt vmcnt(16)
	v_mul_f32_e32 v66, 0x42000000, v66
	v_mul_f32_e32 v67, 0x42000000, v67
	v_mul_f32_e32 v68, 0x42000000, v68
	v_mul_f32_e32 v69, 0x42000000, v69
	v_mul_f32_e32 v70, 0x42000000, v70
	v_mul_f32_e32 v71, 0x42000000, v71
	v_mul_f32_e32 v72, 0x42000000, v72
	v_mul_f32_e32 v73, 0x42000000, v73
	v_mul_f32_e32 v74, 0x42000000, v74
	v_mul_f32_e32 v75, 0x42000000, v75
	v_mul_f32_e32 v76, 0x42000000, v76
	v_mul_f32_e32 v77, 0x42000000, v77
	v_mul_f32_e32 v78, 0x42000000, v78
	v_mul_f32_e32 v79, 0x42000000, v79
	v_mul_f32_e32 v80, 0x42000000, v80
	v_mul_f32_e32 v81, 0x42000000, v81
	v_cvt_pk_fp8_f32 v162, v66, v67
	v_cvt_pk_fp8_f32 v163, v70, v71
	v_cvt_pk_fp8_f32 v164, v74, v75
	v_cvt_pk_fp8_f32 v165, v78, v79
	v_cvt_pk_fp8_f32 v162, v68, v69 op_sel:[0,0,1]
	v_cvt_pk_fp8_f32 v163, v72, v73 op_sel:[0,0,1]
	v_cvt_pk_fp8_f32 v164, v76, v77 op_sel:[0,0,1]
	v_cvt_pk_fp8_f32 v165, v80, v81 op_sel:[0,0,1]
	s_waitcnt vmcnt(0)
	v_mul_f32_e32 v82, 0x42000000, v82
	v_mul_f32_e32 v83, 0x42000000, v83
	v_mul_f32_e32 v84, 0x42000000, v84
	v_mul_f32_e32 v85, 0x42000000, v85
	v_mul_f32_e32 v86, 0x42000000, v86
	v_mul_f32_e32 v87, 0x42000000, v87
	v_mul_f32_e32 v88, 0x42000000, v88
	v_mul_f32_e32 v89, 0x42000000, v89
	v_mul_f32_e32 v90, 0x42000000, v90
	v_mul_f32_e32 v91, 0x42000000, v91
	v_mul_f32_e32 v92, 0x42000000, v92
	v_mul_f32_e32 v93, 0x42000000, v93
	v_mul_f32_e32 v94, 0x42000000, v94
	v_mul_f32_e32 v95, 0x42000000, v95
	v_mul_f32_e32 v96, 0x42000000, v96
	v_mul_f32_e32 v97, 0x42000000, v97
	v_cvt_pk_fp8_f32 v166, v82, v83
	v_cvt_pk_fp8_f32 v167, v86, v87
	v_cvt_pk_fp8_f32 v168, v90, v91
	v_cvt_pk_fp8_f32 v169, v94, v95
	v_cvt_pk_fp8_f32 v166, v84, v85 op_sel:[0,0,1]
	v_cvt_pk_fp8_f32 v167, v88, v89 op_sel:[0,0,1]
	v_cvt_pk_fp8_f32 v168, v92, v93 op_sel:[0,0,1]
	v_cvt_pk_fp8_f32 v169, v96, v97 op_sel:[0,0,1]
	s_mov_b32 vcc_lo, 0xaaaaaaaa
	s_mov_b32 vcc_hi, 0xaaaaaaaa
	s_nop 1
	v_cndmask_b32_dpp v170, v154, v158, vcc quad_perm:[1,0,3,2] row_mask:0xf bank_mask:0xf
	v_cndmask_b32_dpp v174, v162, v166, vcc quad_perm:[1,0,3,2] row_mask:0xf bank_mask:0xf
	v_cndmask_b32_dpp v171, v155, v159, vcc quad_perm:[1,0,3,2] row_mask:0xf bank_mask:0xf
	v_cndmask_b32_dpp v175, v163, v167, vcc quad_perm:[1,0,3,2] row_mask:0xf bank_mask:0xf
	v_cndmask_b32_dpp v172, v156, v160, vcc quad_perm:[1,0,3,2] row_mask:0xf bank_mask:0xf
	v_cndmask_b32_dpp v176, v164, v168, vcc quad_perm:[1,0,3,2] row_mask:0xf bank_mask:0xf
	v_cndmask_b32_dpp v173, v157, v161, vcc quad_perm:[1,0,3,2] row_mask:0xf bank_mask:0xf
	v_cndmask_b32_dpp v177, v165, v169, vcc quad_perm:[1,0,3,2] row_mask:0xf bank_mask:0xf
	s_mov_b32 vcc_lo, 0x55555555
	s_mov_b32 vcc_hi, 0x55555555
	s_nop 1
	v_cndmask_b32_dpp v154, v158, v154, vcc quad_perm:[1,0,3,2] row_mask:0xf bank_mask:0xf
	v_cndmask_b32_dpp v162, v166, v162, vcc quad_perm:[1,0,3,2] row_mask:0xf bank_mask:0xf
	v_cndmask_b32_dpp v155, v159, v155, vcc quad_perm:[1,0,3,2] row_mask:0xf bank_mask:0xf
	v_cndmask_b32_dpp v163, v167, v163, vcc quad_perm:[1,0,3,2] row_mask:0xf bank_mask:0xf
	v_cndmask_b32_dpp v156, v160, v156, vcc quad_perm:[1,0,3,2] row_mask:0xf bank_mask:0xf
	v_cndmask_b32_dpp v164, v168, v164, vcc quad_perm:[1,0,3,2] row_mask:0xf bank_mask:0xf
	v_cndmask_b32_dpp v157, v161, v157, vcc quad_perm:[1,0,3,2] row_mask:0xf bank_mask:0xf
	v_cndmask_b32_dpp v165, v169, v165, vcc quad_perm:[1,0,3,2] row_mask:0xf bank_mask:0xf
	s_mov_b32 vcc_lo, 0xcccccccc
	s_mov_b32 vcc_hi, 0xcccccccc
	s_nop 1
	v_cndmask_b32_dpp v158, v154, v162, vcc quad_perm:[2,3,0,1] row_mask:0xf bank_mask:0xf
	v_cndmask_b32_dpp v166, v170, v174, vcc quad_perm:[2,3,0,1] row_mask:0xf bank_mask:0xf
	v_cndmask_b32_dpp v159, v155, v163, vcc quad_perm:[2,3,0,1] row_mask:0xf bank_mask:0xf
	v_cndmask_b32_dpp v167, v171, v175, vcc quad_perm:[2,3,0,1] row_mask:0xf bank_mask:0xf
	v_cndmask_b32_dpp v160, v156, v164, vcc quad_perm:[2,3,0,1] row_mask:0xf bank_mask:0xf
	v_cndmask_b32_dpp v168, v172, v176, vcc quad_perm:[2,3,0,1] row_mask:0xf bank_mask:0xf
	v_cndmask_b32_dpp v161, v157, v165, vcc quad_perm:[2,3,0,1] row_mask:0xf bank_mask:0xf
	v_cndmask_b32_dpp v169, v173, v177, vcc quad_perm:[2,3,0,1] row_mask:0xf bank_mask:0xf
	s_mov_b32 vcc_lo, 0x33333333
	s_mov_b32 vcc_hi, 0x33333333
	s_nop 1
	v_cndmask_b32_dpp v154, v162, v154, vcc quad_perm:[2,3,0,1] row_mask:0xf bank_mask:0xf
	v_cndmask_b32_dpp v170, v174, v170, vcc quad_perm:[2,3,0,1] row_mask:0xf bank_mask:0xf
	v_cndmask_b32_dpp v155, v163, v155, vcc quad_perm:[2,3,0,1] row_mask:0xf bank_mask:0xf
	v_cndmask_b32_dpp v171, v175, v171, vcc quad_perm:[2,3,0,1] row_mask:0xf bank_mask:0xf
	v_cndmask_b32_dpp v156, v164, v156, vcc quad_perm:[2,3,0,1] row_mask:0xf bank_mask:0xf
	v_cndmask_b32_dpp v172, v176, v172, vcc quad_perm:[2,3,0,1] row_mask:0xf bank_mask:0xf
	v_cndmask_b32_dpp v157, v165, v157, vcc quad_perm:[2,3,0,1] row_mask:0xf bank_mask:0xf
	v_cndmask_b32_dpp v173, v177, v173, vcc quad_perm:[2,3,0,1] row_mask:0xf bank_mask:0xf
	global_store_dwordx4 v179, v[154:157], s[82:83] sc1
	global_store_dwordx4 v180, v[170:173], s[82:83] sc1
	global_store_dwordx4 v181, v[158:161], s[82:83] sc1
	global_store_dwordx4 v190, v[166:169], s[82:83] sc1
	v_readlane_b32 s2, v239, 0
	s_lshr_b32 s2, s2, 6
	s_add_i32 s2, s2, 6
	s_cmp_gt_u32 s2, 13
	s_cbranch_scc1 .Lhw_seam4_done
	s_add_i32 s2, s2, 56
	s_mul_i32 s2, s2, s74
	v_readlane_b32 s9, v239, 23
	s_lshr_b32 s9, s9, 3
	s_add_i32 s2, s2, s9
	s_cmp_gt_u32 s2, 24575
	s_cbranch_scc1 .Lhw_seam4_done
	v_mbcnt_lo_u32_b32 v178, -1, 0
	v_mbcnt_hi_u32_b32 v178, -1, v178
	v_and_b32_e32 v179, 60, v178
	v_lshlrev_b32_e32 v179, 10, v179
	v_and_b32_e32 v180, 3, v178
	v_lshl_or_b32 v179, v180, 4, v179
	v_add_u32_e32 v180, 0x400, v179
	v_add_u32_e32 v181, 0x800, v179
	v_add_u32_e32 v190, 0xc00, v179
	v_lshlrev_b32_e32 v178, 2, v178
	s_cmp_lt_u32 s2, 16384
	s_cbranch_scc0 .Lhw_dn_s4_1
	s_lshr_b32 s9, s2, 9
	s_bfe_u32 s32, s2, 0x40005
	s_and_b32 s53, s2, 31
	s_lshl_b32 s69, s9, 23
	s_lshl_b32 s100, s32, 19
	s_add_i32 s69, s69, s100
	s_lshl_b32 s100, s53, 8
	s_add_i32 s69, s69, s100
	s_lshl_b32 s98, s9, 11
	s_bfe_u32 s100, s53, 0x30001
	s_lshl_b32 s100, s100, 8
	s_add_i32 s98, s98, s100
	s_lshr_b32 s100, s53, 4
	s_lshl_b32 s100, s100, 7
	s_add_i32 s98, s98, s100
	s_and_b32 s100, s53, 1
	s_lshl_b32 s100, s100, 6
	s_add_i32 s98, s98, s100
	s_lshl_b32 s98, s98, 10
	s_lshl_b32 s100, s32, 6
	s_add_i32 s98, s98, s100
	s_add_i32 s98, s98, 0x2000000
	v_readlane_b32 s82, v239, 11
	v_readlane_b32 s83, v239, 12
	s_movk_i32 s89, 8192
	s_branch .Lhw_go_s4_1

.Lhw_go_s5_0:
	s_add_u32 s100, s82, s69
	s_addc_u32 s101, s83, 0
	v_readlane_b32 s82, v239, 44
	v_readlane_b32 s83, v239, 45
	s_add_u32 s82, s82, s98
	s_addc_u32 s83, s83, 0
	global_load_dword v34, v178, s[100:101] nt
	s_add_u32 s100, s100, s89
	s_addc_u32 s101, s101, 0
	global_load_dword v35, v178, s[100:101] nt
	s_add_u32 s100, s100, s89
	s_addc_u32 s101, s101, 0
	global_load_dword v36, v178, s[100:101] nt
	s_add_u32 s100, s100, s89
	s_addc_u32 s101, s101, 0
	global_load_dword v37, v178, s[100:101] nt
	s_add_u32 s100, s100, s89
	s_addc_u32 s101, s101, 0
	global_load_dword v38, v178, s[100:101] nt
	s_add_u32 s100, s100, s89
	s_addc_u32 s101, s101, 0
	global_load_dword v39, v178, s[100:101] nt
	s_add_u32 s100, s100, s89
	s_addc_u32 s101, s101, 0
	global_load_dword v40, v178, s[100:101] nt
	s_add_u32 s100, s100, s89
	s_addc_u32 s101, s101, 0
	global_load_dword v41, v178, s[100:101] nt
	s_add_u32 s100, s100, s89
	s_addc_u32 s101, s101, 0
	global_load_dword v42, v178, s[100:101] nt
	s_add_u32 s100, s100, s89
	s_addc_u32 s101, s101, 0
	global_load_dword v43, v178, s[100:101] nt
	s_add_u32 s100, s100, s89
	s_addc_u32 s101, s101, 0
	global_load_dword v44, v178, s[100:101] nt
	s_add_u32 s100, s100, s89
	s_addc_u32 s101, s101, 0
	global_load_dword v45, v178, s[100:101] nt
	s_add_u32 s100, s100, s89
	s_addc_u32 s101, s101, 0
	global_load_dword v46, v178, s[100:101] nt
	s_add_u32 s100, s100, s89
	s_addc_u32 s101, s101, 0
	global_load_dword v47, v178, s[100:101] nt
	s_add_u32 s100, s100, s89
	s_addc_u32 s101, s101, 0
	global_load_dword v48, v178, s[100:101] nt
	s_add_u32 s100, s100, s89
	s_addc_u32 s101, s101, 0
	global_load_dword v49, v178, s[100:101] nt
	s_add_u32 s100, s100, s89
	s_addc_u32 s101, s101, 0
	global_load_dword v50, v178, s[100:101] nt
	s_add_u32 s100, s100, s89
	s_addc_u32 s101, s101, 0
	global_load_dword v51, v178, s[100:101] nt
	s_add_u32 s100, s100, s89
	s_addc_u32 s101, s101, 0
	global_load_dword v52, v178, s[100:101] nt
	s_add_u32 s100, s100, s89
	s_addc_u32 s101, s101, 0
	global_load_dword v53, v178, s[100:101] nt
	s_add_u32 s100, s100, s89
	s_addc_u32 s101, s101, 0
	global_load_dword v54, v178, s[100:101] nt
	s_add_u32 s100, s100, s89
	s_addc_u32 s101, s101, 0
	global_load_dword v55, v178, s[100:101] nt
	s_add_u32 s100, s100, s89
	s_addc_u32 s101, s101, 0
	global_load_dword v56, v178, s[100:101] nt
	s_add_u32 s100, s100, s89
	s_addc_u32 s101, s101, 0
	global_load_dword v57, v178, s[100:101] nt
	s_add_u32 s100, s100, s89
	s_addc_u32 s101, s101, 0
	global_load_dword v58, v178, s[100:101] nt
	s_add_u32 s100, s100, s89
	s_addc_u32 s101, s101, 0
	global_load_dword v59, v178, s[100:101] nt
	s_add_u32 s100, s100, s89
	s_addc_u32 s101, s101, 0
	global_load_dword v60, v178, s[100:101] nt
	s_add_u32 s100, s100, s89
	s_addc_u32 s101, s101, 0
	global_load_dword v61, v178, s[100:101] nt
	s_add_u32 s100, s100, s89
	s_addc_u32 s101, s101, 0
	global_load_dword v62, v178, s[100:101] nt
	s_add_u32 s100, s100, s89
	s_addc_u32 s101, s101, 0
	global_load_dword v63, v178, s[100:101] nt
	s_add_u32 s100, s100, s89
	s_addc_u32 s101, s101, 0
	global_load_dword v64, v178, s[100:101] nt
	s_add_u32 s100, s100, s89
	s_addc_u32 s101, s101, 0
	global_load_dword v65, v178, s[100:101] nt
	s_add_u32 s100, s100, s89
	s_addc_u32 s101, s101, 0
	global_load_dword v66, v178, s[100:101] nt
	s_add_u32 s100, s100, s89
	s_addc_u32 s101, s101, 0
	global_load_dword v67, v178, s[100:101] nt
	s_add_u32 s100, s100, s89
	s_addc_u32 s101, s101, 0
	global_load_dword v68, v178, s[100:101] nt
	s_add_u32 s100, s100, s89
	s_addc_u32 s101, s101, 0
	global_load_dword v69, v178, s[100:101] nt
	s_add_u32 s100, s100, s89
	s_addc_u32 s101, s101, 0
	global_load_dword v70, v178, s[100:101] nt
	s_add_u32 s100, s100, s89
	s_addc_u32 s101, s101, 0
	global_load_dword v71, v178, s[100:101] nt
	s_add_u32 s100, s100, s89
	s_addc_u32 s101, s101, 0
	global_load_dword v72, v178, s[100:101] nt
	s_add_u32 s100, s100, s89
	s_addc_u32 s101, s101, 0
	global_load_dword v73, v178, s[100:101] nt
	s_add_u32 s100, s100, s89
	s_addc_u32 s101, s101, 0
	global_load_dword v74, v178, s[100:101] nt
	s_add_u32 s100, s100, s89
	s_addc_u32 s101, s101, 0
	global_load_dword v75, v178, s[100:101] nt
	s_add_u32 s100, s100, s89
	s_addc_u32 s101, s101, 0
	global_load_dword v76, v178, s[100:101] nt
	s_add_u32 s100, s100, s89
	s_addc_u32 s101, s101, 0
	global_load_dword v77, v178, s[100:101] nt
	s_add_u32 s100, s100, s89
	s_addc_u32 s101, s101, 0
	global_load_dword v78, v178, s[100:101] nt
	s_add_u32 s100, s100, s89
	s_addc_u32 s101, s101, 0
	global_load_dword v79, v178, s[100:101] nt
	s_add_u32 s100, s100, s89
	s_addc_u32 s101, s101, 0
	global_load_dword v80, v178, s[100:101] nt
	s_add_u32 s100, s100, s89
	s_addc_u32 s101, s101, 0
	global_load_dword v81, v178, s[100:101] nt
	s_add_u32 s100, s100, s89
	s_addc_u32 s101, s101, 0
	global_load_dword v82, v178, s[100:101] nt
	s_add_u32 s100, s100, s89
	s_addc_u32 s101, s101, 0
	global_load_dword v83, v178, s[100:101] nt
	s_add_u32 s100, s100, s89
	s_addc_u32 s101, s101, 0
	global_load_dword v84, v178, s[100:101] nt
	s_add_u32 s100, s100, s89
	s_addc_u32 s101, s101, 0
	global_load_dword v85, v178, s[100:101] nt
	s_add_u32 s100, s100, s89
	s_addc_u32 s101, s101, 0
	global_load_dword v86, v178, s[100:101] nt
	s_add_u32 s100, s100, s89
	s_addc_u32 s101, s101, 0
	global_load_dword v87, v178, s[100:101] nt
	s_add_u32 s100, s100, s89
	s_addc_u32 s101, s101, 0
	global_load_dword v88, v178, s[100:101] nt
	s_add_u32 s100, s100, s89
	s_addc_u32 s101, s101, 0
	global_load_dword v89, v178, s[100:101] nt
	s_add_u32 s100, s100, s89
	s_addc_u32 s101, s101, 0
	global_load_dword v90, v178, s[100:101] nt
	s_add_u32 s100, s100, s89
	s_addc_u32 s101, s101, 0
	global_load_dword v91, v178, s[100:101] nt
	s_add_u32 s100, s100, s89
	s_addc_u32 s101, s101, 0
	global_load_dword v92, v178, s[100:101] nt
	s_add_u32 s100, s100, s89
	s_addc_u32 s101, s101, 0
	global_load_dword v93, v178, s[100:101] nt
	s_add_u32 s100, s100, s89
	s_addc_u32 s101, s101, 0
	global_load_dword v94, v178, s[100:101] nt
	s_add_u32 s100, s100, s89
	s_addc_u32 s101, s101, 0
	global_load_dword v95, v178, s[100:101] nt
	s_add_u32 s100, s100, s89
	s_addc_u32 s101, s101, 0
	global_load_dword v96, v178, s[100:101] nt
	s_add_u32 s100, s100, s89
	s_addc_u32 s101, s101, 0
	global_load_dword v97, v178, s[100:101] nt
	s_add_u32 s100, s100, s89
	s_addc_u32 s101, s101, 0
	s_waitcnt vmcnt(48)
	v_mul_f32_e32 v34, 0x42000000, v34
	v_mul_f32_e32 v35, 0x42000000, v35
	v_mul_f32_e32 v36, 0x42000000, v36
	v_mul_f32_e32 v37, 0x42000000, v37
	v_mul_f32_e32 v38, 0x42000000, v38
	v_mul_f32_e32 v39, 0x42000000, v39
	v_mul_f32_e32 v40, 0x42000000, v40
	v_mul_f32_e32 v41, 0x42000000, v41
	v_mul_f32_e32 v42, 0x42000000, v42
	v_mul_f32_e32 v43, 0x42000000, v43
	v_mul_f32_e32 v44, 0x42000000, v44
	v_mul_f32_e32 v45, 0x42000000, v45
	v_mul_f32_e32 v46, 0x42000000, v46
	v_mul_f32_e32 v47, 0x42000000, v47
	v_mul_f32_e32 v48, 0x42000000, v48
	v_mul_f32_e32 v49, 0x42000000, v49
	v_cvt_pk_fp8_f32 v154, v34, v35
	v_cvt_pk_fp8_f32 v155, v38, v39
	v_cvt_pk_fp8_f32 v156, v42, v43
	v_cvt_pk_fp8_f32 v157, v46, v47
	v_cvt_pk_fp8_f32 v154, v36, v37 op_sel:[0,0,1]
	v_cvt_pk_fp8_f32 v155, v40, v41 op_sel:[0,0,1]
	v_cvt_pk_fp8_f32 v156, v44, v45 op_sel:[0,0,1]
	v_cvt_pk_fp8_f32 v157, v48, v49 op_sel:[0,0,1]
	s_waitcnt vmcnt(32)
	v_mul_f32_e32 v50, 0x42000000, v50
	v_mul_f32_e32 v51, 0x42000000, v51
	v_mul_f32_e32 v52, 0x42000000, v52
	v_mul_f32_e32 v53, 0x42000000, v53
	v_mul_f32_e32 v54, 0x42000000, v54
	v_mul_f32_e32 v55, 0x42000000, v55
	v_mul_f32_e32 v56, 0x42000000, v56
	v_mul_f32_e32 v57, 0x42000000, v57
	v_mul_f32_e32 v58, 0x42000000, v58
	v_mul_f32_e32 v59, 0x42000000, v59
	v_mul_f32_e32 v60, 0x42000000, v60
	v_mul_f32_e32 v61, 0x42000000, v61
	v_mul_f32_e32 v62, 0x42000000, v62
	v_mul_f32_e32 v63, 0x42000000, v63
	v_mul_f32_e32 v64, 0x42000000, v64
	v_mul_f32_e32 v65, 0x42000000, v65
	v_cvt_pk_fp8_f32 v158, v50, v51
	v_cvt_pk_fp8_f32 v159, v54, v55
	v_cvt_pk_fp8_f32 v160, v58, v59
	v_cvt_pk_fp8_f32 v161, v62, v63
	v_cvt_pk_fp8_f32 v158, v52, v53 op_sel:[0,0,1]
	v_cvt_pk_fp8_f32 v159, v56, v57 op_sel:[0,0,1]
	v_cvt_pk_fp8_f32 v160, v60, v61 op_sel:[0,0,1]
	v_cvt_pk_fp8_f32 v161, v64, v65 op_sel:[0,0,1]
	s_waitcnt vmcnt(16)
	v_mul_f32_e32 v66, 0x42000000, v66
	v_mul_f32_e32 v67, 0x42000000, v67
	v_mul_f32_e32 v68, 0x42000000, v68
	v_mul_f32_e32 v69, 0x42000000, v69
	v_mul_f32_e32 v70, 0x42000000, v70
	v_mul_f32_e32 v71, 0x42000000, v71
	v_mul_f32_e32 v72, 0x42000000, v72
	v_mul_f32_e32 v73, 0x42000000, v73
	v_mul_f32_e32 v74, 0x42000000, v74
	v_mul_f32_e32 v75, 0x42000000, v75
	v_mul_f32_e32 v76, 0x42000000, v76
	v_mul_f32_e32 v77, 0x42000000, v77
	v_mul_f32_e32 v78, 0x42000000, v78
	v_mul_f32_e32 v79, 0x42000000, v79
	v_mul_f32_e32 v80, 0x42000000, v80
	v_mul_f32_e32 v81, 0x42000000, v81
	v_cvt_pk_fp8_f32 v162, v66, v67
	v_cvt_pk_fp8_f32 v163, v70, v71
	v_cvt_pk_fp8_f32 v164, v74, v75
	v_cvt_pk_fp8_f32 v165, v78, v79
	v_cvt_pk_fp8_f32 v162, v68, v69 op_sel:[0,0,1]
	v_cvt_pk_fp8_f32 v163, v72, v73 op_sel:[0,0,1]
	v_cvt_pk_fp8_f32 v164, v76, v77 op_sel:[0,0,1]
	v_cvt_pk_fp8_f32 v165, v80, v81 op_sel:[0,0,1]
	s_waitcnt vmcnt(0)
	v_mul_f32_e32 v82, 0x42000000, v82
	v_mul_f32_e32 v83, 0x42000000, v83
	v_mul_f32_e32 v84, 0x42000000, v84
	v_mul_f32_e32 v85, 0x42000000, v85
	v_mul_f32_e32 v86, 0x42000000, v86
	v_mul_f32_e32 v87, 0x42000000, v87
	v_mul_f32_e32 v88, 0x42000000, v88
	v_mul_f32_e32 v89, 0x42000000, v89
	v_mul_f32_e32 v90, 0x42000000, v90
	v_mul_f32_e32 v91, 0x42000000, v91
	v_mul_f32_e32 v92, 0x42000000, v92
	v_mul_f32_e32 v93, 0x42000000, v93
	v_mul_f32_e32 v94, 0x42000000, v94
	v_mul_f32_e32 v95, 0x42000000, v95
	v_mul_f32_e32 v96, 0x42000000, v96
	v_mul_f32_e32 v97, 0x42000000, v97
	v_cvt_pk_fp8_f32 v166, v82, v83
	v_cvt_pk_fp8_f32 v167, v86, v87
	v_cvt_pk_fp8_f32 v168, v90, v91
	v_cvt_pk_fp8_f32 v169, v94, v95
	v_cvt_pk_fp8_f32 v166, v84, v85 op_sel:[0,0,1]
	v_cvt_pk_fp8_f32 v167, v88, v89 op_sel:[0,0,1]
	v_cvt_pk_fp8_f32 v168, v92, v93 op_sel:[0,0,1]
	v_cvt_pk_fp8_f32 v169, v96, v97 op_sel:[0,0,1]
	s_mov_b32 vcc_lo, 0xaaaaaaaa
	s_mov_b32 vcc_hi, 0xaaaaaaaa
	s_nop 1
	v_cndmask_b32_dpp v170, v154, v158, vcc quad_perm:[1,0,3,2] row_mask:0xf bank_mask:0xf
	v_cndmask_b32_dpp v174, v162, v166, vcc quad_perm:[1,0,3,2] row_mask:0xf bank_mask:0xf
	v_cndmask_b32_dpp v171, v155, v159, vcc quad_perm:[1,0,3,2] row_mask:0xf bank_mask:0xf
	v_cndmask_b32_dpp v175, v163, v167, vcc quad_perm:[1,0,3,2] row_mask:0xf bank_mask:0xf
	v_cndmask_b32_dpp v172, v156, v160, vcc quad_perm:[1,0,3,2] row_mask:0xf bank_mask:0xf
	v_cndmask_b32_dpp v176, v164, v168, vcc quad_perm:[1,0,3,2] row_mask:0xf bank_mask:0xf
	v_cndmask_b32_dpp v173, v157, v161, vcc quad_perm:[1,0,3,2] row_mask:0xf bank_mask:0xf
	v_cndmask_b32_dpp v177, v165, v169, vcc quad_perm:[1,0,3,2] row_mask:0xf bank_mask:0xf
	s_mov_b32 vcc_lo, 0x55555555
	s_mov_b32 vcc_hi, 0x55555555
	s_nop 1
	v_cndmask_b32_dpp v154, v158, v154, vcc quad_perm:[1,0,3,2] row_mask:0xf bank_mask:0xf
	v_cndmask_b32_dpp v162, v166, v162, vcc quad_perm:[1,0,3,2] row_mask:0xf bank_mask:0xf
	v_cndmask_b32_dpp v155, v159, v155, vcc quad_perm:[1,0,3,2] row_mask:0xf bank_mask:0xf
	v_cndmask_b32_dpp v163, v167, v163, vcc quad_perm:[1,0,3,2] row_mask:0xf bank_mask:0xf
	v_cndmask_b32_dpp v156, v160, v156, vcc quad_perm:[1,0,3,2] row_mask:0xf bank_mask:0xf
	v_cndmask_b32_dpp v164, v168, v164, vcc quad_perm:[1,0,3,2] row_mask:0xf bank_mask:0xf
	v_cndmask_b32_dpp v157, v161, v157, vcc quad_perm:[1,0,3,2] row_mask:0xf bank_mask:0xf
	v_cndmask_b32_dpp v165, v169, v165, vcc quad_perm:[1,0,3,2] row_mask:0xf bank_mask:0xf
	s_mov_b32 vcc_lo, 0xcccccccc
	s_mov_b32 vcc_hi, 0xcccccccc
	s_nop 1
	v_cndmask_b32_dpp v158, v154, v162, vcc quad_perm:[2,3,0,1] row_mask:0xf bank_mask:0xf
	v_cndmask_b32_dpp v166, v170, v174, vcc quad_perm:[2,3,0,1] row_mask:0xf bank_mask:0xf
	v_cndmask_b32_dpp v159, v155, v163, vcc quad_perm:[2,3,0,1] row_mask:0xf bank_mask:0xf
	v_cndmask_b32_dpp v167, v171, v175, vcc quad_perm:[2,3,0,1] row_mask:0xf bank_mask:0xf
	v_cndmask_b32_dpp v160, v156, v164, vcc quad_perm:[2,3,0,1] row_mask:0xf bank_mask:0xf
	v_cndmask_b32_dpp v168, v172, v176, vcc quad_perm:[2,3,0,1] row_mask:0xf bank_mask:0xf
	v_cndmask_b32_dpp v161, v157, v165, vcc quad_perm:[2,3,0,1] row_mask:0xf bank_mask:0xf
	v_cndmask_b32_dpp v169, v173, v177, vcc quad_perm:[2,3,0,1] row_mask:0xf bank_mask:0xf
	s_mov_b32 vcc_lo, 0x33333333
	s_mov_b32 vcc_hi, 0x33333333
	s_nop 1
	v_cndmask_b32_dpp v154, v162, v154, vcc quad_perm:[2,3,0,1] row_mask:0xf bank_mask:0xf
	v_cndmask_b32_dpp v170, v174, v170, vcc quad_perm:[2,3,0,1] row_mask:0xf bank_mask:0xf
	v_cndmask_b32_dpp v155, v163, v155, vcc quad_perm:[2,3,0,1] row_mask:0xf bank_mask:0xf
	v_cndmask_b32_dpp v171, v175, v171, vcc quad_perm:[2,3,0,1] row_mask:0xf bank_mask:0xf
	v_cndmask_b32_dpp v156, v164, v156, vcc quad_perm:[2,3,0,1] row_mask:0xf bank_mask:0xf
	v_cndmask_b32_dpp v172, v176, v172, vcc quad_perm:[2,3,0,1] row_mask:0xf bank_mask:0xf
	v_cndmask_b32_dpp v157, v165, v157, vcc quad_perm:[2,3,0,1] row_mask:0xf bank_mask:0xf
	v_cndmask_b32_dpp v173, v177, v173, vcc quad_perm:[2,3,0,1] row_mask:0xf bank_mask:0xf
	global_store_dwordx4 v179, v[154:157], s[82:83] sc1
	global_store_dwordx4 v180, v[170:173], s[82:83] sc1
	global_store_dwordx4 v181, v[158:161], s[82:83] sc1
	global_store_dwordx4 v190, v[166:169], s[82:83] sc1
	v_readlane_b32 s2, v239, 0
	s_lshr_b32 s2, s2, 6
	s_add_i32 s2, s2, 6
	s_cmp_gt_u32 s2, 13
	s_cbranch_scc1 .Lhw_seam5_done
	s_add_i32 s2, s2, 70
	s_mul_i32 s2, s2, s74
	v_readlane_b32 s9, v239, 23
	s_lshr_b32 s9, s9, 3
	s_add_i32 s2, s2, s9
	s_cmp_gt_u32 s2, 24575
	s_cbranch_scc1 .Lhw_seam5_done
	v_mbcnt_lo_u32_b32 v178, -1, 0
	v_mbcnt_hi_u32_b32 v178, -1, v178
	v_and_b32_e32 v179, 60, v178
	v_lshlrev_b32_e32 v179, 10, v179
	v_and_b32_e32 v180, 3, v178
	v_lshl_or_b32 v179, v180, 4, v179
	v_add_u32_e32 v180, 0x400, v179
	v_add_u32_e32 v181, 0x800, v179
	v_add_u32_e32 v190, 0xc00, v179
	v_lshlrev_b32_e32 v178, 2, v178
	s_cmp_lt_u32 s2, 16384
	s_cbranch_scc0 .Lhw_dn_s5_1
	s_lshr_b32 s9, s2, 9
	s_bfe_u32 s32, s2, 0x40005
	s_and_b32 s53, s2, 31
	s_lshl_b32 s69, s9, 23
	s_lshl_b32 s100, s32, 19
	s_add_i32 s69, s69, s100
	s_lshl_b32 s100, s53, 8
	s_add_i32 s69, s69, s100
	s_lshl_b32 s98, s9, 11
	s_bfe_u32 s100, s53, 0x30001
	s_lshl_b32 s100, s100, 8
	s_add_i32 s98, s98, s100
	s_lshr_b32 s100, s53, 4
	s_lshl_b32 s100, s100, 7
	s_add_i32 s98, s98, s100
	s_and_b32 s100, s53, 1
	s_lshl_b32 s100, s100, 6
	s_add_i32 s98, s98, s100
	s_lshl_b32 s98, s98, 10
	s_lshl_b32 s100, s32, 6
	s_add_i32 s98, s98, s100
	s_add_i32 s98, s98, 0x2000000
	v_readlane_b32 s82, v239, 11
	v_readlane_b32 s83, v239, 12
	s_movk_i32 s89, 8192
	s_branch .Lhw_go_s5_1

.Lhw_go_s6_0:
	s_add_u32 s100, s82, s69
	s_addc_u32 s101, s83, 0
	v_readlane_b32 s82, v239, 44
	v_readlane_b32 s83, v239, 45
	s_add_u32 s82, s82, s98
	s_addc_u32 s83, s83, 0
	global_load_dword v34, v178, s[100:101] nt
	s_add_u32 s100, s100, s89
	s_addc_u32 s101, s101, 0
	global_load_dword v35, v178, s[100:101] nt
	s_add_u32 s100, s100, s89
	s_addc_u32 s101, s101, 0
	global_load_dword v36, v178, s[100:101] nt
	s_add_u32 s100, s100, s89
	s_addc_u32 s101, s101, 0
	global_load_dword v37, v178, s[100:101] nt
	s_add_u32 s100, s100, s89
	s_addc_u32 s101, s101, 0
	global_load_dword v38, v178, s[100:101] nt
	s_add_u32 s100, s100, s89
	s_addc_u32 s101, s101, 0
	global_load_dword v39, v178, s[100:101] nt
	s_add_u32 s100, s100, s89
	s_addc_u32 s101, s101, 0
	global_load_dword v40, v178, s[100:101] nt
	s_add_u32 s100, s100, s89
	s_addc_u32 s101, s101, 0
	global_load_dword v41, v178, s[100:101] nt
	s_add_u32 s100, s100, s89
	s_addc_u32 s101, s101, 0
	global_load_dword v42, v178, s[100:101] nt
	s_add_u32 s100, s100, s89
	s_addc_u32 s101, s101, 0
	global_load_dword v43, v178, s[100:101] nt
	s_add_u32 s100, s100, s89
	s_addc_u32 s101, s101, 0
	global_load_dword v44, v178, s[100:101] nt
	s_add_u32 s100, s100, s89
	s_addc_u32 s101, s101, 0
	global_load_dword v45, v178, s[100:101] nt
	s_add_u32 s100, s100, s89
	s_addc_u32 s101, s101, 0
	global_load_dword v46, v178, s[100:101] nt
	s_add_u32 s100, s100, s89
	s_addc_u32 s101, s101, 0
	global_load_dword v47, v178, s[100:101] nt
	s_add_u32 s100, s100, s89
	s_addc_u32 s101, s101, 0
	global_load_dword v48, v178, s[100:101] nt
	s_add_u32 s100, s100, s89
	s_addc_u32 s101, s101, 0
	global_load_dword v49, v178, s[100:101] nt
	s_add_u32 s100, s100, s89
	s_addc_u32 s101, s101, 0
	global_load_dword v50, v178, s[100:101] nt
	s_add_u32 s100, s100, s89
	s_addc_u32 s101, s101, 0
	global_load_dword v51, v178, s[100:101] nt
	s_add_u32 s100, s100, s89
	s_addc_u32 s101, s101, 0
	global_load_dword v52, v178, s[100:101] nt
	s_add_u32 s100, s100, s89
	s_addc_u32 s101, s101, 0
	global_load_dword v53, v178, s[100:101] nt
	s_add_u32 s100, s100, s89
	s_addc_u32 s101, s101, 0
	global_load_dword v54, v178, s[100:101] nt
	s_add_u32 s100, s100, s89
	s_addc_u32 s101, s101, 0
	global_load_dword v55, v178, s[100:101] nt
	s_add_u32 s100, s100, s89
	s_addc_u32 s101, s101, 0
	global_load_dword v56, v178, s[100:101] nt
	s_add_u32 s100, s100, s89
	s_addc_u32 s101, s101, 0
	global_load_dword v57, v178, s[100:101] nt
	s_add_u32 s100, s100, s89
	s_addc_u32 s101, s101, 0
	global_load_dword v58, v178, s[100:101] nt
	s_add_u32 s100, s100, s89
	s_addc_u32 s101, s101, 0
	global_load_dword v59, v178, s[100:101] nt
	s_add_u32 s100, s100, s89
	s_addc_u32 s101, s101, 0
	global_load_dword v60, v178, s[100:101] nt
	s_add_u32 s100, s100, s89
	s_addc_u32 s101, s101, 0
	global_load_dword v61, v178, s[100:101] nt
	s_add_u32 s100, s100, s89
	s_addc_u32 s101, s101, 0
	global_load_dword v62, v178, s[100:101] nt
	s_add_u32 s100, s100, s89
	s_addc_u32 s101, s101, 0
	global_load_dword v63, v178, s[100:101] nt
	s_add_u32 s100, s100, s89
	s_addc_u32 s101, s101, 0
	global_load_dword v64, v178, s[100:101] nt
	s_add_u32 s100, s100, s89
	s_addc_u32 s101, s101, 0
	global_load_dword v65, v178, s[100:101] nt
	s_add_u32 s100, s100, s89
	s_addc_u32 s101, s101, 0
	global_load_dword v66, v178, s[100:101] nt
	s_add_u32 s100, s100, s89
	s_addc_u32 s101, s101, 0
	global_load_dword v67, v178, s[100:101] nt
	s_add_u32 s100, s100, s89
	s_addc_u32 s101, s101, 0
	global_load_dword v68, v178, s[100:101] nt
	s_add_u32 s100, s100, s89
	s_addc_u32 s101, s101, 0
	global_load_dword v69, v178, s[100:101] nt
	s_add_u32 s100, s100, s89
	s_addc_u32 s101, s101, 0
	global_load_dword v70, v178, s[100:101] nt
	s_add_u32 s100, s100, s89
	s_addc_u32 s101, s101, 0
	global_load_dword v71, v178, s[100:101] nt
	s_add_u32 s100, s100, s89
	s_addc_u32 s101, s101, 0
	global_load_dword v72, v178, s[100:101] nt
	s_add_u32 s100, s100, s89
	s_addc_u32 s101, s101, 0
	global_load_dword v73, v178, s[100:101] nt
	s_add_u32 s100, s100, s89
	s_addc_u32 s101, s101, 0
	global_load_dword v74, v178, s[100:101] nt
	s_add_u32 s100, s100, s89
	s_addc_u32 s101, s101, 0
	global_load_dword v75, v178, s[100:101] nt
	s_add_u32 s100, s100, s89
	s_addc_u32 s101, s101, 0
	global_load_dword v76, v178, s[100:101] nt
	s_add_u32 s100, s100, s89
	s_addc_u32 s101, s101, 0
	global_load_dword v77, v178, s[100:101] nt
	s_add_u32 s100, s100, s89
	s_addc_u32 s101, s101, 0
	global_load_dword v78, v178, s[100:101] nt
	s_add_u32 s100, s100, s89
	s_addc_u32 s101, s101, 0
	global_load_dword v79, v178, s[100:101] nt
	s_add_u32 s100, s100, s89
	s_addc_u32 s101, s101, 0
	global_load_dword v80, v178, s[100:101] nt
	s_add_u32 s100, s100, s89
	s_addc_u32 s101, s101, 0
	global_load_dword v81, v178, s[100:101] nt
	s_add_u32 s100, s100, s89
	s_addc_u32 s101, s101, 0
	global_load_dword v82, v178, s[100:101] nt
	s_add_u32 s100, s100, s89
	s_addc_u32 s101, s101, 0
	global_load_dword v83, v178, s[100:101] nt
	s_add_u32 s100, s100, s89
	s_addc_u32 s101, s101, 0
	global_load_dword v84, v178, s[100:101] nt
	s_add_u32 s100, s100, s89
	s_addc_u32 s101, s101, 0
	global_load_dword v85, v178, s[100:101] nt
	s_add_u32 s100, s100, s89
	s_addc_u32 s101, s101, 0
	global_load_dword v86, v178, s[100:101] nt
	s_add_u32 s100, s100, s89
	s_addc_u32 s101, s101, 0
	global_load_dword v87, v178, s[100:101] nt
	s_add_u32 s100, s100, s89
	s_addc_u32 s101, s101, 0
	global_load_dword v88, v178, s[100:101] nt
	s_add_u32 s100, s100, s89
	s_addc_u32 s101, s101, 0
	global_load_dword v89, v178, s[100:101] nt
	s_add_u32 s100, s100, s89
	s_addc_u32 s101, s101, 0
	global_load_dword v90, v178, s[100:101] nt
	s_add_u32 s100, s100, s89
	s_addc_u32 s101, s101, 0
	global_load_dword v91, v178, s[100:101] nt
	s_add_u32 s100, s100, s89
	s_addc_u32 s101, s101, 0
	global_load_dword v92, v178, s[100:101] nt
	s_add_u32 s100, s100, s89
	s_addc_u32 s101, s101, 0
	global_load_dword v93, v178, s[100:101] nt
	s_add_u32 s100, s100, s89
	s_addc_u32 s101, s101, 0
	global_load_dword v94, v178, s[100:101] nt
	s_add_u32 s100, s100, s89
	s_addc_u32 s101, s101, 0
	global_load_dword v95, v178, s[100:101] nt
	s_add_u32 s100, s100, s89
	s_addc_u32 s101, s101, 0
	global_load_dword v96, v178, s[100:101] nt
	s_add_u32 s100, s100, s89
	s_addc_u32 s101, s101, 0
	global_load_dword v97, v178, s[100:101] nt
	s_add_u32 s100, s100, s89
	s_addc_u32 s101, s101, 0
	s_waitcnt vmcnt(48)
	v_mul_f32_e32 v34, 0x42000000, v34
	v_mul_f32_e32 v35, 0x42000000, v35
	v_mul_f32_e32 v36, 0x42000000, v36
	v_mul_f32_e32 v37, 0x42000000, v37
	v_mul_f32_e32 v38, 0x42000000, v38
	v_mul_f32_e32 v39, 0x42000000, v39
	v_mul_f32_e32 v40, 0x42000000, v40
	v_mul_f32_e32 v41, 0x42000000, v41
	v_mul_f32_e32 v42, 0x42000000, v42
	v_mul_f32_e32 v43, 0x42000000, v43
	v_mul_f32_e32 v44, 0x42000000, v44
	v_mul_f32_e32 v45, 0x42000000, v45
	v_mul_f32_e32 v46, 0x42000000, v46
	v_mul_f32_e32 v47, 0x42000000, v47
	v_mul_f32_e32 v48, 0x42000000, v48
	v_mul_f32_e32 v49, 0x42000000, v49
	v_cvt_pk_fp8_f32 v154, v34, v35
	v_cvt_pk_fp8_f32 v155, v38, v39
	v_cvt_pk_fp8_f32 v156, v42, v43
	v_cvt_pk_fp8_f32 v157, v46, v47
	v_cvt_pk_fp8_f32 v154, v36, v37 op_sel:[0,0,1]
	v_cvt_pk_fp8_f32 v155, v40, v41 op_sel:[0,0,1]
	v_cvt_pk_fp8_f32 v156, v44, v45 op_sel:[0,0,1]
	v_cvt_pk_fp8_f32 v157, v48, v49 op_sel:[0,0,1]
	s_waitcnt vmcnt(32)
	v_mul_f32_e32 v50, 0x42000000, v50
	v_mul_f32_e32 v51, 0x42000000, v51
	v_mul_f32_e32 v52, 0x42000000, v52
	v_mul_f32_e32 v53, 0x42000000, v53
	v_mul_f32_e32 v54, 0x42000000, v54
	v_mul_f32_e32 v55, 0x42000000, v55
	v_mul_f32_e32 v56, 0x42000000, v56
	v_mul_f32_e32 v57, 0x42000000, v57
	v_mul_f32_e32 v58, 0x42000000, v58
	v_mul_f32_e32 v59, 0x42000000, v59
	v_mul_f32_e32 v60, 0x42000000, v60
	v_mul_f32_e32 v61, 0x42000000, v61
	v_mul_f32_e32 v62, 0x42000000, v62
	v_mul_f32_e32 v63, 0x42000000, v63
	v_mul_f32_e32 v64, 0x42000000, v64
	v_mul_f32_e32 v65, 0x42000000, v65
	v_cvt_pk_fp8_f32 v158, v50, v51
	v_cvt_pk_fp8_f32 v159, v54, v55
	v_cvt_pk_fp8_f32 v160, v58, v59
	v_cvt_pk_fp8_f32 v161, v62, v63
	v_cvt_pk_fp8_f32 v158, v52, v53 op_sel:[0,0,1]
	v_cvt_pk_fp8_f32 v159, v56, v57 op_sel:[0,0,1]
	v_cvt_pk_fp8_f32 v160, v60, v61 op_sel:[0,0,1]
	v_cvt_pk_fp8_f32 v161, v64, v65 op_sel:[0,0,1]
	s_waitcnt vmcnt(16)
	v_mul_f32_e32 v66, 0x42000000, v66
	v_mul_f32_e32 v67, 0x42000000, v67
	v_mul_f32_e32 v68, 0x42000000, v68
	v_mul_f32_e32 v69, 0x42000000, v69
	v_mul_f32_e32 v70, 0x42000000, v70
	v_mul_f32_e32 v71, 0x42000000, v71
	v_mul_f32_e32 v72, 0x42000000, v72
	v_mul_f32_e32 v73, 0x42000000, v73
	v_mul_f32_e32 v74, 0x42000000, v74
	v_mul_f32_e32 v75, 0x42000000, v75
	v_mul_f32_e32 v76, 0x42000000, v76
	v_mul_f32_e32 v77, 0x42000000, v77
	v_mul_f32_e32 v78, 0x42000000, v78
	v_mul_f32_e32 v79, 0x42000000, v79
	v_mul_f32_e32 v80, 0x42000000, v80
	v_mul_f32_e32 v81, 0x42000000, v81
	v_cvt_pk_fp8_f32 v162, v66, v67
	v_cvt_pk_fp8_f32 v163, v70, v71
	v_cvt_pk_fp8_f32 v164, v74, v75
	v_cvt_pk_fp8_f32 v165, v78, v79
	v_cvt_pk_fp8_f32 v162, v68, v69 op_sel:[0,0,1]
	v_cvt_pk_fp8_f32 v163, v72, v73 op_sel:[0,0,1]
	v_cvt_pk_fp8_f32 v164, v76, v77 op_sel:[0,0,1]
	v_cvt_pk_fp8_f32 v165, v80, v81 op_sel:[0,0,1]
	s_waitcnt vmcnt(0)
	v_mul_f32_e32 v82, 0x42000000, v82
	v_mul_f32_e32 v83, 0x42000000, v83
	v_mul_f32_e32 v84, 0x42000000, v84
	v_mul_f32_e32 v85, 0x42000000, v85
	v_mul_f32_e32 v86, 0x42000000, v86
	v_mul_f32_e32 v87, 0x42000000, v87
	v_mul_f32_e32 v88, 0x42000000, v88
	v_mul_f32_e32 v89, 0x42000000, v89
	v_mul_f32_e32 v90, 0x42000000, v90
	v_mul_f32_e32 v91, 0x42000000, v91
	v_mul_f32_e32 v92, 0x42000000, v92
	v_mul_f32_e32 v93, 0x42000000, v93
	v_mul_f32_e32 v94, 0x42000000, v94
	v_mul_f32_e32 v95, 0x42000000, v95
	v_mul_f32_e32 v96, 0x42000000, v96
	v_mul_f32_e32 v97, 0x42000000, v97
	v_cvt_pk_fp8_f32 v166, v82, v83
	v_cvt_pk_fp8_f32 v167, v86, v87
	v_cvt_pk_fp8_f32 v168, v90, v91
	v_cvt_pk_fp8_f32 v169, v94, v95
	v_cvt_pk_fp8_f32 v166, v84, v85 op_sel:[0,0,1]
	v_cvt_pk_fp8_f32 v167, v88, v89 op_sel:[0,0,1]
	v_cvt_pk_fp8_f32 v168, v92, v93 op_sel:[0,0,1]
	v_cvt_pk_fp8_f32 v169, v96, v97 op_sel:[0,0,1]
	s_mov_b32 vcc_lo, 0xaaaaaaaa
	s_mov_b32 vcc_hi, 0xaaaaaaaa
	s_nop 1
	v_cndmask_b32_dpp v170, v154, v158, vcc quad_perm:[1,0,3,2] row_mask:0xf bank_mask:0xf
	v_cndmask_b32_dpp v174, v162, v166, vcc quad_perm:[1,0,3,2] row_mask:0xf bank_mask:0xf
	v_cndmask_b32_dpp v171, v155, v159, vcc quad_perm:[1,0,3,2] row_mask:0xf bank_mask:0xf
	v_cndmask_b32_dpp v175, v163, v167, vcc quad_perm:[1,0,3,2] row_mask:0xf bank_mask:0xf
	v_cndmask_b32_dpp v172, v156, v160, vcc quad_perm:[1,0,3,2] row_mask:0xf bank_mask:0xf
	v_cndmask_b32_dpp v176, v164, v168, vcc quad_perm:[1,0,3,2] row_mask:0xf bank_mask:0xf
	v_cndmask_b32_dpp v173, v157, v161, vcc quad_perm:[1,0,3,2] row_mask:0xf bank_mask:0xf
	v_cndmask_b32_dpp v177, v165, v169, vcc quad_perm:[1,0,3,2] row_mask:0xf bank_mask:0xf
	s_mov_b32 vcc_lo, 0x55555555
	s_mov_b32 vcc_hi, 0x55555555
	s_nop 1
	v_cndmask_b32_dpp v154, v158, v154, vcc quad_perm:[1,0,3,2] row_mask:0xf bank_mask:0xf
	v_cndmask_b32_dpp v162, v166, v162, vcc quad_perm:[1,0,3,2] row_mask:0xf bank_mask:0xf
	v_cndmask_b32_dpp v155, v159, v155, vcc quad_perm:[1,0,3,2] row_mask:0xf bank_mask:0xf
	v_cndmask_b32_dpp v163, v167, v163, vcc quad_perm:[1,0,3,2] row_mask:0xf bank_mask:0xf
	v_cndmask_b32_dpp v156, v160, v156, vcc quad_perm:[1,0,3,2] row_mask:0xf bank_mask:0xf
	v_cndmask_b32_dpp v164, v168, v164, vcc quad_perm:[1,0,3,2] row_mask:0xf bank_mask:0xf
	v_cndmask_b32_dpp v157, v161, v157, vcc quad_perm:[1,0,3,2] row_mask:0xf bank_mask:0xf
	v_cndmask_b32_dpp v165, v169, v165, vcc quad_perm:[1,0,3,2] row_mask:0xf bank_mask:0xf
	s_mov_b32 vcc_lo, 0xcccccccc
	s_mov_b32 vcc_hi, 0xcccccccc
	s_nop 1
	v_cndmask_b32_dpp v158, v154, v162, vcc quad_perm:[2,3,0,1] row_mask:0xf bank_mask:0xf
	v_cndmask_b32_dpp v166, v170, v174, vcc quad_perm:[2,3,0,1] row_mask:0xf bank_mask:0xf
	v_cndmask_b32_dpp v159, v155, v163, vcc quad_perm:[2,3,0,1] row_mask:0xf bank_mask:0xf
	v_cndmask_b32_dpp v167, v171, v175, vcc quad_perm:[2,3,0,1] row_mask:0xf bank_mask:0xf
	v_cndmask_b32_dpp v160, v156, v164, vcc quad_perm:[2,3,0,1] row_mask:0xf bank_mask:0xf
	v_cndmask_b32_dpp v168, v172, v176, vcc quad_perm:[2,3,0,1] row_mask:0xf bank_mask:0xf
	v_cndmask_b32_dpp v161, v157, v165, vcc quad_perm:[2,3,0,1] row_mask:0xf bank_mask:0xf
	v_cndmask_b32_dpp v169, v173, v177, vcc quad_perm:[2,3,0,1] row_mask:0xf bank_mask:0xf
	s_mov_b32 vcc_lo, 0x33333333
	s_mov_b32 vcc_hi, 0x33333333
	s_nop 1
	v_cndmask_b32_dpp v154, v162, v154, vcc quad_perm:[2,3,0,1] row_mask:0xf bank_mask:0xf
	v_cndmask_b32_dpp v170, v174, v170, vcc quad_perm:[2,3,0,1] row_mask:0xf bank_mask:0xf
	v_cndmask_b32_dpp v155, v163, v155, vcc quad_perm:[2,3,0,1] row_mask:0xf bank_mask:0xf
	v_cndmask_b32_dpp v171, v175, v171, vcc quad_perm:[2,3,0,1] row_mask:0xf bank_mask:0xf
	v_cndmask_b32_dpp v156, v164, v156, vcc quad_perm:[2,3,0,1] row_mask:0xf bank_mask:0xf
	v_cndmask_b32_dpp v172, v176, v172, vcc quad_perm:[2,3,0,1] row_mask:0xf bank_mask:0xf
	v_cndmask_b32_dpp v157, v165, v157, vcc quad_perm:[2,3,0,1] row_mask:0xf bank_mask:0xf
	v_cndmask_b32_dpp v173, v177, v173, vcc quad_perm:[2,3,0,1] row_mask:0xf bank_mask:0xf
	global_store_dwordx4 v179, v[154:157], s[82:83] sc1
	global_store_dwordx4 v180, v[170:173], s[82:83] sc1
	global_store_dwordx4 v181, v[158:161], s[82:83] sc1
	global_store_dwordx4 v190, v[166:169], s[82:83] sc1
	v_readlane_b32 s2, v239, 0
	s_lshr_b32 s2, s2, 6
	s_add_i32 s2, s2, 6
	s_cmp_gt_u32 s2, 11
	s_cbranch_scc1 .Lhw_seam6_done
	s_add_i32 s2, s2, 84
	s_mul_i32 s2, s2, s74
	v_readlane_b32 s9, v239, 23
	s_lshr_b32 s9, s9, 3
	s_add_i32 s2, s2, s9
	s_cmp_gt_u32 s2, 24575
	s_cbranch_scc1 .Lhw_seam6_done
	v_mbcnt_lo_u32_b32 v178, -1, 0
	v_mbcnt_hi_u32_b32 v178, -1, v178
	v_and_b32_e32 v179, 60, v178
	v_lshlrev_b32_e32 v179, 10, v179
	v_and_b32_e32 v180, 3, v178
	v_lshl_or_b32 v179, v180, 4, v179
	v_add_u32_e32 v180, 0x400, v179
	v_add_u32_e32 v181, 0x800, v179
	v_add_u32_e32 v190, 0xc00, v179
	v_lshlrev_b32_e32 v178, 2, v178
	s_cmp_lt_u32 s2, 16384
	s_cbranch_scc0 .Lhw_dn_s6_1
	s_lshr_b32 s9, s2, 9
	s_bfe_u32 s32, s2, 0x40005
	s_and_b32 s53, s2, 31
	s_lshl_b32 s69, s9, 23
	s_lshl_b32 s100, s32, 19
	s_add_i32 s69, s69, s100
	s_lshl_b32 s100, s53, 8
	s_add_i32 s69, s69, s100
	s_lshl_b32 s98, s9, 11
	s_bfe_u32 s100, s53, 0x30001
	s_lshl_b32 s100, s100, 8
	s_add_i32 s98, s98, s100
	s_lshr_b32 s100, s53, 4
	s_lshl_b32 s100, s100, 7
	s_add_i32 s98, s98, s100
	s_and_b32 s100, s53, 1
	s_lshl_b32 s100, s100, 6
	s_add_i32 s98, s98, s100
	s_lshl_b32 s98, s98, 10
	s_lshl_b32 s100, s32, 6
	s_add_i32 s98, s98, s100
	s_add_i32 s98, s98, 0x2000000
	v_readlane_b32 s82, v239, 11
	v_readlane_b32 s83, v239, 12
	s_movk_i32 s89, 8192
	s_branch .Lhw_go_s6_1
